# prologue GEMV main loop and one weight-copy loop: counted vmcnt waits and first uses sunk below the last load of each 16-load batch (all loads issued before the first wait)
# speedup vs baseline: 1.0039x; 1.0021x over previous
.LBB0_15:
	v_add_co_u32_e32 v70, vcc, s39, v4
	global_load_dwordx4 v[130:133], v[4:5], off
	s_nop 0
	v_addc_co_u32_e32 v71, vcc, 0, v5, vcc
	global_load_dwordx4 v[134:137], v[70:71], off
	v_add_co_u32_e32 v70, vcc, s42, v4
	v_add_u32_e32 v138, 0xffff0000, v2
	s_nop 0
	v_addc_co_u32_e32 v71, vcc, 0, v5, vcc
	global_load_dwordx4 v[114:117], v[70:71], off
	v_add_co_u32_e32 v70, vcc, s43, v4
	ds_read_b128 v[138:141], v138
	s_nop 0
	v_addc_co_u32_e32 v71, vcc, 0, v5, vcc
	global_load_dwordx4 v[126:129], v[70:71], off
	v_add_co_u32_e32 v70, vcc, s44, v4
	s_add_i32 s31, s31, 16
	s_nop 0
	v_addc_co_u32_e32 v71, vcc, 0, v5, vcc
	global_load_dwordx4 v[118:121], v[70:71], off
	v_add_co_u32_e32 v70, vcc, s45, v4
	s_cmp_gt_u32 s31, 47
	s_nop 0
	v_addc_co_u32_e32 v71, vcc, 0, v5, vcc
	global_load_dwordx4 v[122:125], v[70:71], off
	v_add_co_u32_e32 v70, vcc, s46, v4
	s_nop 0
	s_nop 0
	v_addc_co_u32_e32 v71, vcc, 0, v5, vcc
	global_load_dwordx4 v[102:105], v[70:71], off
	v_add_co_u32_e32 v70, vcc, s47, v4
	s_nop 0
	s_nop 0
	v_addc_co_u32_e32 v71, vcc, 0, v5, vcc
	global_load_dwordx4 v[110:113], v[70:71], off
	v_add_co_u32_e32 v70, vcc, s48, v4
	s_nop 0
	s_nop 0
	v_addc_co_u32_e32 v71, vcc, 0, v5, vcc
	global_load_dwordx4 v[98:101], v[70:71], off
	v_add_co_u32_e32 v70, vcc, s49, v4
	s_nop 0
	s_nop 0
	v_addc_co_u32_e32 v71, vcc, 0, v5, vcc
	global_load_dwordx4 v[106:109], v[70:71], off
	v_add_co_u32_e32 v70, vcc, s50, v4
	s_nop 0
	s_nop 0
	v_addc_co_u32_e32 v71, vcc, 0, v5, vcc
	global_load_dwordx4 v[82:85], v[70:71], off
	v_add_co_u32_e32 v70, vcc, s51, v4
	s_nop 0
	s_nop 0
	v_addc_co_u32_e32 v71, vcc, 0, v5, vcc
	global_load_dwordx4 v[94:97], v[70:71], off
	v_add_co_u32_e32 v70, vcc, s52, v4
	s_nop 0
	s_nop 0
	v_addc_co_u32_e32 v71, vcc, 0, v5, vcc
	global_load_dwordx4 v[78:81], v[70:71], off
	v_add_co_u32_e32 v70, vcc, s53, v4
	s_nop 0
	s_nop 0
	v_addc_co_u32_e32 v71, vcc, 0, v5, vcc
	global_load_dwordx4 v[86:89], v[70:71], off
	v_add_co_u32_e32 v70, vcc, s54, v4
	s_nop 0
	s_nop 0
	v_addc_co_u32_e32 v71, vcc, 0, v5, vcc
	v_add_co_u32_e32 v74, vcc, s55, v4
	global_load_dwordx4 v[70:73], v[70:71], off
	s_nop 0
	v_addc_co_u32_e32 v75, vcc, 0, v5, vcc
	global_load_dwordx4 v[74:77], v[74:75], off
	s_waitcnt vmcnt(14) lgkmcnt(0)
	v_pk_mul_f32 v[142:143], v[136:137], v[138:139] op_sel:[0,1]
	v_pk_mul_f32 v[144:145], v[134:135], v[138:139] op_sel:[0,1]
	v_pk_fma_f32 v[142:143], v[132:133], v[138:139], v[142:143] op_sel_hi:[1,0,1]
	v_pk_fma_f32 v[138:139], v[130:131], v[138:139], v[144:145] op_sel_hi:[1,0,1]
	v_mov_b32_e32 v144, v141
	s_waitcnt vmcnt(12)
	v_pk_mul_f32 v[146:147], v[128:129], v[144:145] op_sel_hi:[1,0]
	v_pk_mul_f32 v[144:145], v[126:127], v[144:145] op_sel_hi:[1,0]
	v_pk_fma_f32 v[146:147], v[116:117], v[140:141], v[146:147] op_sel_hi:[1,0,1]
	v_pk_fma_f32 v[140:141], v[114:115], v[140:141], v[144:145] op_sel_hi:[1,0,1]
	v_pk_add_f32 v[138:139], v[138:139], v[140:141]
	v_pk_add_f32 v[142:143], v[142:143], v[146:147]
	v_pk_add_f32 v[138:139], v[66:67], v[138:139]
	v_add_u32_e32 v66, 0xffff0010, v2
	v_pk_add_f32 v[140:141], v[68:69], v[142:143]
	ds_read_b128 v[66:69], v66
	v_lshl_add_u64 v[4:5], v[4:5], 0, s[10:11]
	s_waitcnt vmcnt(10) lgkmcnt(0)
	v_pk_mul_f32 v[142:143], v[124:125], v[66:67] op_sel:[0,1]
	v_pk_mul_f32 v[144:145], v[122:123], v[66:67] op_sel:[0,1]
	v_pk_fma_f32 v[142:143], v[120:121], v[66:67], v[142:143] op_sel_hi:[1,0,1]
	v_pk_fma_f32 v[66:67], v[118:119], v[66:67], v[144:145] op_sel_hi:[1,0,1]
	v_mov_b32_e32 v144, v69
	s_waitcnt vmcnt(8)
	v_pk_mul_f32 v[146:147], v[112:113], v[144:145] op_sel_hi:[1,0]
	v_pk_mul_f32 v[144:145], v[110:111], v[144:145] op_sel_hi:[1,0]
	v_pk_fma_f32 v[146:147], v[104:105], v[68:69], v[146:147] op_sel_hi:[1,0,1]
	v_pk_fma_f32 v[68:69], v[102:103], v[68:69], v[144:145] op_sel_hi:[1,0,1]
	v_pk_add_f32 v[142:143], v[142:143], v[146:147]
	v_pk_add_f32 v[66:67], v[66:67], v[68:69]
	v_pk_add_f32 v[140:141], v[140:141], v[142:143]
	v_pk_add_f32 v[138:139], v[138:139], v[66:67]
	v_add_u32_e32 v66, 0xffff0020, v2
	ds_read_b128 v[66:69], v66
	s_waitcnt vmcnt(6) lgkmcnt(0)
	v_pk_mul_f32 v[142:143], v[108:109], v[66:67] op_sel:[0,1]
	v_pk_mul_f32 v[144:145], v[106:107], v[66:67] op_sel:[0,1]
	v_pk_fma_f32 v[142:143], v[100:101], v[66:67], v[142:143] op_sel_hi:[1,0,1]
	v_pk_fma_f32 v[66:67], v[98:99], v[66:67], v[144:145] op_sel_hi:[1,0,1]
	v_mov_b32_e32 v144, v69
	s_waitcnt vmcnt(4)
	v_pk_mul_f32 v[146:147], v[96:97], v[144:145] op_sel_hi:[1,0]
	v_pk_mul_f32 v[144:145], v[94:95], v[144:145] op_sel_hi:[1,0]
	v_pk_fma_f32 v[146:147], v[84:85], v[68:69], v[146:147] op_sel_hi:[1,0,1]
	v_pk_fma_f32 v[68:69], v[82:83], v[68:69], v[144:145] op_sel_hi:[1,0,1]
	v_pk_add_f32 v[142:143], v[142:143], v[146:147]
	v_pk_add_f32 v[66:67], v[66:67], v[68:69]
	v_pk_add_f32 v[140:141], v[140:141], v[142:143]
	v_pk_add_f32 v[138:139], v[138:139], v[66:67]
	v_add_u32_e32 v66, 0xffff0030, v2
	ds_read_b128 v[66:69], v66
	s_waitcnt vmcnt(2) lgkmcnt(0)
	v_pk_mul_f32 v[142:143], v[88:89], v[66:67] op_sel:[0,1]
	v_pk_mul_f32 v[144:145], v[86:87], v[66:67] op_sel:[0,1]
	v_pk_fma_f32 v[142:143], v[80:81], v[66:67], v[142:143] op_sel_hi:[1,0,1]
	v_pk_fma_f32 v[66:67], v[78:79], v[66:67], v[144:145] op_sel_hi:[1,0,1]
	v_mov_b32_e32 v144, v69
	s_waitcnt vmcnt(0)
	v_pk_mul_f32 v[146:147], v[76:77], v[144:145] op_sel_hi:[1,0]
	v_pk_mul_f32 v[144:145], v[74:75], v[144:145] op_sel_hi:[1,0]
	v_pk_fma_f32 v[146:147], v[72:73], v[68:69], v[146:147] op_sel_hi:[1,0,1]
	v_pk_fma_f32 v[68:69], v[70:71], v[68:69], v[144:145] op_sel_hi:[1,0,1]
	v_pk_add_f32 v[142:143], v[142:143], v[146:147]
	v_pk_add_f32 v[66:67], v[66:67], v[68:69]
	v_pk_add_f32 v[68:69], v[140:141], v[142:143]
	v_pk_add_f32 v[66:67], v[138:139], v[66:67]
	v_add_u32_e32 v138, 0xffff1000, v2
	ds_read_b128 v[138:141], v138
	s_waitcnt lgkmcnt(0)
	v_pk_mul_f32 v[142:143], v[136:137], v[138:139] op_sel:[0,1]
	v_pk_mul_f32 v[144:145], v[134:135], v[138:139] op_sel:[0,1]
	v_pk_fma_f32 v[142:143], v[132:133], v[138:139], v[142:143] op_sel_hi:[1,0,1]
	v_pk_fma_f32 v[138:139], v[130:131], v[138:139], v[144:145] op_sel_hi:[1,0,1]
	v_mov_b32_e32 v144, v141
	v_pk_mul_f32 v[146:147], v[128:129], v[144:145] op_sel_hi:[1,0]
	v_pk_mul_f32 v[144:145], v[126:127], v[144:145] op_sel_hi:[1,0]
	v_pk_fma_f32 v[146:147], v[116:117], v[140:141], v[146:147] op_sel_hi:[1,0,1]
	v_pk_fma_f32 v[140:141], v[114:115], v[140:141], v[144:145] op_sel_hi:[1,0,1]
	v_pk_add_f32 v[142:143], v[142:143], v[146:147]
	v_pk_add_f32 v[138:139], v[138:139], v[140:141]
	v_pk_add_f32 v[140:141], v[64:65], v[142:143]
	v_pk_add_f32 v[138:139], v[62:63], v[138:139]
	v_add_u32_e32 v62, 0xffff1010, v2
	ds_read_b128 v[62:65], v62
	s_waitcnt lgkmcnt(0)
	v_pk_mul_f32 v[142:143], v[124:125], v[62:63] op_sel:[0,1]
	v_pk_mul_f32 v[144:145], v[122:123], v[62:63] op_sel:[0,1]
	v_pk_fma_f32 v[142:143], v[120:121], v[62:63], v[142:143] op_sel_hi:[1,0,1]
	v_pk_fma_f32 v[62:63], v[118:119], v[62:63], v[144:145] op_sel_hi:[1,0,1]
	v_mov_b32_e32 v144, v65
	v_pk_mul_f32 v[146:147], v[112:113], v[144:145] op_sel_hi:[1,0]
	v_pk_mul_f32 v[144:145], v[110:111], v[144:145] op_sel_hi:[1,0]
	v_pk_fma_f32 v[146:147], v[104:105], v[64:65], v[146:147] op_sel_hi:[1,0,1]
	v_pk_fma_f32 v[64:65], v[102:103], v[64:65], v[144:145] op_sel_hi:[1,0,1]
	v_pk_add_f32 v[142:143], v[142:143], v[146:147]
	v_pk_add_f32 v[62:63], v[62:63], v[64:65]
	v_pk_add_f32 v[140:141], v[140:141], v[142:143]
	v_pk_add_f32 v[138:139], v[138:139], v[62:63]
	v_add_u32_e32 v62, 0xffff1020, v2
	ds_read_b128 v[62:65], v62
	s_waitcnt lgkmcnt(0)
	v_pk_mul_f32 v[142:143], v[108:109], v[62:63] op_sel:[0,1]
	v_pk_mul_f32 v[144:145], v[106:107], v[62:63] op_sel:[0,1]
	v_pk_fma_f32 v[142:143], v[100:101], v[62:63], v[142:143] op_sel_hi:[1,0,1]
	v_pk_fma_f32 v[62:63], v[98:99], v[62:63], v[144:145] op_sel_hi:[1,0,1]
	v_mov_b32_e32 v144, v65
	v_pk_mul_f32 v[146:147], v[96:97], v[144:145] op_sel_hi:[1,0]
	v_pk_mul_f32 v[144:145], v[94:95], v[144:145] op_sel_hi:[1,0]
	v_pk_fma_f32 v[146:147], v[84:85], v[64:65], v[146:147] op_sel_hi:[1,0,1]
	v_pk_fma_f32 v[64:65], v[82:83], v[64:65], v[144:145] op_sel_hi:[1,0,1]
	v_pk_add_f32 v[142:143], v[142:143], v[146:147]
	v_pk_add_f32 v[62:63], v[62:63], v[64:65]
	v_pk_add_f32 v[140:141], v[140:141], v[142:143]
	v_pk_add_f32 v[138:139], v[138:139], v[62:63]
	v_add_u32_e32 v62, 0xffff1030, v2
	ds_read_b128 v[62:65], v62
	s_waitcnt lgkmcnt(0)
	v_pk_mul_f32 v[142:143], v[88:89], v[62:63] op_sel:[0,1]
	v_pk_mul_f32 v[144:145], v[86:87], v[62:63] op_sel:[0,1]
	v_pk_fma_f32 v[142:143], v[80:81], v[62:63], v[142:143] op_sel_hi:[1,0,1]
	v_pk_fma_f32 v[62:63], v[78:79], v[62:63], v[144:145] op_sel_hi:[1,0,1]
	v_mov_b32_e32 v144, v65
	v_pk_mul_f32 v[146:147], v[76:77], v[144:145] op_sel_hi:[1,0]
	v_pk_mul_f32 v[144:145], v[74:75], v[144:145] op_sel_hi:[1,0]
	v_pk_fma_f32 v[146:147], v[72:73], v[64:65], v[146:147] op_sel_hi:[1,0,1]
	v_pk_fma_f32 v[64:65], v[70:71], v[64:65], v[144:145] op_sel_hi:[1,0,1]
	v_pk_add_f32 v[142:143], v[142:143], v[146:147]
	v_pk_add_f32 v[62:63], v[62:63], v[64:65]
	v_pk_add_f32 v[64:65], v[140:141], v[142:143]
	v_pk_add_f32 v[62:63], v[138:139], v[62:63]
	v_add_u32_e32 v138, 0xffff2000, v2
	ds_read_b128 v[138:141], v138
	s_waitcnt lgkmcnt(0)
	v_pk_mul_f32 v[142:143], v[136:137], v[138:139] op_sel:[0,1]
	v_pk_mul_f32 v[144:145], v[134:135], v[138:139] op_sel:[0,1]
	v_pk_fma_f32 v[142:143], v[132:133], v[138:139], v[142:143] op_sel_hi:[1,0,1]
	v_pk_fma_f32 v[138:139], v[130:131], v[138:139], v[144:145] op_sel_hi:[1,0,1]
	v_mov_b32_e32 v144, v141
	v_pk_mul_f32 v[146:147], v[128:129], v[144:145] op_sel_hi:[1,0]
	v_pk_mul_f32 v[144:145], v[126:127], v[144:145] op_sel_hi:[1,0]
	v_pk_fma_f32 v[146:147], v[116:117], v[140:141], v[146:147] op_sel_hi:[1,0,1]
	v_pk_fma_f32 v[140:141], v[114:115], v[140:141], v[144:145] op_sel_hi:[1,0,1]
	v_pk_add_f32 v[142:143], v[142:143], v[146:147]
	v_pk_add_f32 v[138:139], v[138:139], v[140:141]
	v_pk_add_f32 v[140:141], v[60:61], v[142:143]
	v_pk_add_f32 v[138:139], v[58:59], v[138:139]
	v_add_u32_e32 v58, 0xffff2010, v2
	ds_read_b128 v[58:61], v58
	s_waitcnt lgkmcnt(0)
	v_pk_mul_f32 v[142:143], v[124:125], v[58:59] op_sel:[0,1]
	v_pk_mul_f32 v[144:145], v[122:123], v[58:59] op_sel:[0,1]
	v_pk_fma_f32 v[142:143], v[120:121], v[58:59], v[142:143] op_sel_hi:[1,0,1]
	v_pk_fma_f32 v[58:59], v[118:119], v[58:59], v[144:145] op_sel_hi:[1,0,1]
	v_mov_b32_e32 v144, v61
	v_pk_mul_f32 v[146:147], v[112:113], v[144:145] op_sel_hi:[1,0]
	v_pk_mul_f32 v[144:145], v[110:111], v[144:145] op_sel_hi:[1,0]
	v_pk_fma_f32 v[146:147], v[104:105], v[60:61], v[146:147] op_sel_hi:[1,0,1]
	v_pk_fma_f32 v[60:61], v[102:103], v[60:61], v[144:145] op_sel_hi:[1,0,1]
	v_pk_add_f32 v[142:143], v[142:143], v[146:147]
	v_pk_add_f32 v[58:59], v[58:59], v[60:61]
	v_pk_add_f32 v[140:141], v[140:141], v[142:143]
	v_pk_add_f32 v[138:139], v[138:139], v[58:59]
	v_add_u32_e32 v58, 0xffff2020, v2
	ds_read_b128 v[58:61], v58
	s_waitcnt lgkmcnt(0)
	v_pk_mul_f32 v[142:143], v[108:109], v[58:59] op_sel:[0,1]
	v_pk_mul_f32 v[144:145], v[106:107], v[58:59] op_sel:[0,1]
	v_pk_fma_f32 v[142:143], v[100:101], v[58:59], v[142:143] op_sel_hi:[1,0,1]
	v_pk_fma_f32 v[58:59], v[98:99], v[58:59], v[144:145] op_sel_hi:[1,0,1]
	v_mov_b32_e32 v144, v61
	v_pk_mul_f32 v[146:147], v[96:97], v[144:145] op_sel_hi:[1,0]
	v_pk_mul_f32 v[144:145], v[94:95], v[144:145] op_sel_hi:[1,0]
	v_pk_fma_f32 v[146:147], v[84:85], v[60:61], v[146:147] op_sel_hi:[1,0,1]
	v_pk_fma_f32 v[60:61], v[82:83], v[60:61], v[144:145] op_sel_hi:[1,0,1]
	v_pk_add_f32 v[142:143], v[142:143], v[146:147]
	v_pk_add_f32 v[58:59], v[58:59], v[60:61]
	v_pk_add_f32 v[140:141], v[140:141], v[142:143]
	v_pk_add_f32 v[138:139], v[138:139], v[58:59]
	v_add_u32_e32 v58, 0xffff2030, v2
	ds_read_b128 v[58:61], v58
	s_waitcnt lgkmcnt(0)
	v_pk_mul_f32 v[142:143], v[88:89], v[58:59] op_sel:[0,1]
	v_pk_mul_f32 v[144:145], v[86:87], v[58:59] op_sel:[0,1]
	v_pk_fma_f32 v[142:143], v[80:81], v[58:59], v[142:143] op_sel_hi:[1,0,1]
	v_pk_fma_f32 v[58:59], v[78:79], v[58:59], v[144:145] op_sel_hi:[1,0,1]
	v_mov_b32_e32 v144, v61
	v_pk_mul_f32 v[146:147], v[76:77], v[144:145] op_sel_hi:[1,0]
	v_pk_mul_f32 v[144:145], v[74:75], v[144:145] op_sel_hi:[1,0]
	v_pk_fma_f32 v[146:147], v[72:73], v[60:61], v[146:147] op_sel_hi:[1,0,1]
	v_pk_fma_f32 v[60:61], v[70:71], v[60:61], v[144:145] op_sel_hi:[1,0,1]
	v_pk_add_f32 v[142:143], v[142:143], v[146:147]
	v_pk_add_f32 v[58:59], v[58:59], v[60:61]
	v_pk_add_f32 v[60:61], v[140:141], v[142:143]
	v_pk_add_f32 v[58:59], v[138:139], v[58:59]
	v_add_u32_e32 v138, 0xffff3000, v2
	ds_read_b128 v[138:141], v138
	s_waitcnt lgkmcnt(0)
	v_pk_mul_f32 v[142:143], v[136:137], v[138:139] op_sel:[0,1]
	v_pk_mul_f32 v[144:145], v[134:135], v[138:139] op_sel:[0,1]
	v_pk_fma_f32 v[142:143], v[132:133], v[138:139], v[142:143] op_sel_hi:[1,0,1]
	v_pk_fma_f32 v[138:139], v[130:131], v[138:139], v[144:145] op_sel_hi:[1,0,1]
	v_mov_b32_e32 v144, v141
	v_pk_mul_f32 v[146:147], v[128:129], v[144:145] op_sel_hi:[1,0]
	v_pk_mul_f32 v[144:145], v[126:127], v[144:145] op_sel_hi:[1,0]
	v_pk_fma_f32 v[146:147], v[116:117], v[140:141], v[146:147] op_sel_hi:[1,0,1]
	v_pk_fma_f32 v[140:141], v[114:115], v[140:141], v[144:145] op_sel_hi:[1,0,1]
	v_pk_add_f32 v[142:143], v[142:143], v[146:147]
	v_pk_add_f32 v[138:139], v[138:139], v[140:141]
	v_pk_add_f32 v[140:141], v[56:57], v[142:143]
	v_pk_add_f32 v[138:139], v[54:55], v[138:139]
	v_add_u32_e32 v54, 0xffff3010, v2
	ds_read_b128 v[54:57], v54
	s_waitcnt lgkmcnt(0)
	v_pk_mul_f32 v[142:143], v[124:125], v[54:55] op_sel:[0,1]
	v_pk_mul_f32 v[144:145], v[122:123], v[54:55] op_sel:[0,1]
	v_pk_fma_f32 v[142:143], v[120:121], v[54:55], v[142:143] op_sel_hi:[1,0,1]
	v_pk_fma_f32 v[54:55], v[118:119], v[54:55], v[144:145] op_sel_hi:[1,0,1]
	v_mov_b32_e32 v144, v57
	v_pk_mul_f32 v[146:147], v[112:113], v[144:145] op_sel_hi:[1,0]
	v_pk_mul_f32 v[144:145], v[110:111], v[144:145] op_sel_hi:[1,0]
	v_pk_fma_f32 v[146:147], v[104:105], v[56:57], v[146:147] op_sel_hi:[1,0,1]
	v_pk_fma_f32 v[56:57], v[102:103], v[56:57], v[144:145] op_sel_hi:[1,0,1]
	v_pk_add_f32 v[142:143], v[142:143], v[146:147]
	v_pk_add_f32 v[54:55], v[54:55], v[56:57]
	v_pk_add_f32 v[140:141], v[140:141], v[142:143]
	v_pk_add_f32 v[138:139], v[138:139], v[54:55]
	v_add_u32_e32 v54, 0xffff3020, v2
	ds_read_b128 v[54:57], v54
	s_waitcnt lgkmcnt(0)
	v_pk_mul_f32 v[142:143], v[108:109], v[54:55] op_sel:[0,1]
	v_pk_mul_f32 v[144:145], v[106:107], v[54:55] op_sel:[0,1]
	v_pk_fma_f32 v[142:143], v[100:101], v[54:55], v[142:143] op_sel_hi:[1,0,1]
	v_pk_fma_f32 v[54:55], v[98:99], v[54:55], v[144:145] op_sel_hi:[1,0,1]
	v_mov_b32_e32 v144, v57
	v_pk_mul_f32 v[146:147], v[96:97], v[144:145] op_sel_hi:[1,0]
	v_pk_mul_f32 v[144:145], v[94:95], v[144:145] op_sel_hi:[1,0]
	v_pk_fma_f32 v[146:147], v[84:85], v[56:57], v[146:147] op_sel_hi:[1,0,1]
	v_pk_fma_f32 v[56:57], v[82:83], v[56:57], v[144:145] op_sel_hi:[1,0,1]
	v_pk_add_f32 v[142:143], v[142:143], v[146:147]
	v_pk_add_f32 v[54:55], v[54:55], v[56:57]
	v_pk_add_f32 v[140:141], v[140:141], v[142:143]
	v_pk_add_f32 v[138:139], v[138:139], v[54:55]
	v_add_u32_e32 v54, 0xffff3030, v2
	ds_read_b128 v[54:57], v54
	s_waitcnt lgkmcnt(0)
	v_pk_mul_f32 v[142:143], v[88:89], v[54:55] op_sel:[0,1]
	v_pk_mul_f32 v[144:145], v[86:87], v[54:55] op_sel:[0,1]
	v_pk_fma_f32 v[142:143], v[80:81], v[54:55], v[142:143] op_sel_hi:[1,0,1]
	v_pk_fma_f32 v[54:55], v[78:79], v[54:55], v[144:145] op_sel_hi:[1,0,1]
	v_mov_b32_e32 v144, v57
	v_pk_mul_f32 v[146:147], v[76:77], v[144:145] op_sel_hi:[1,0]
	v_pk_mul_f32 v[144:145], v[74:75], v[144:145] op_sel_hi:[1,0]
	v_pk_fma_f32 v[146:147], v[72:73], v[56:57], v[146:147] op_sel_hi:[1,0,1]
	v_pk_fma_f32 v[56:57], v[70:71], v[56:57], v[144:145] op_sel_hi:[1,0,1]
	v_pk_add_f32 v[142:143], v[142:143], v[146:147]
	v_pk_add_f32 v[54:55], v[54:55], v[56:57]
	v_pk_add_f32 v[56:57], v[140:141], v[142:143]
	v_pk_add_f32 v[54:55], v[138:139], v[54:55]
	v_add_u32_e32 v138, 0xffff4000, v2
	ds_read_b128 v[138:141], v138
	s_waitcnt lgkmcnt(0)
	v_pk_mul_f32 v[142:143], v[136:137], v[138:139] op_sel:[0,1]
	v_pk_mul_f32 v[144:145], v[134:135], v[138:139] op_sel:[0,1]
	v_pk_fma_f32 v[142:143], v[132:133], v[138:139], v[142:143] op_sel_hi:[1,0,1]
	v_pk_fma_f32 v[138:139], v[130:131], v[138:139], v[144:145] op_sel_hi:[1,0,1]
	v_mov_b32_e32 v144, v141
	v_pk_mul_f32 v[146:147], v[128:129], v[144:145] op_sel_hi:[1,0]
	v_pk_mul_f32 v[144:145], v[126:127], v[144:145] op_sel_hi:[1,0]
	v_pk_fma_f32 v[146:147], v[116:117], v[140:141], v[146:147] op_sel_hi:[1,0,1]
	v_pk_fma_f32 v[140:141], v[114:115], v[140:141], v[144:145] op_sel_hi:[1,0,1]
	v_pk_add_f32 v[142:143], v[142:143], v[146:147]
	v_pk_add_f32 v[138:139], v[138:139], v[140:141]
	v_pk_add_f32 v[140:141], v[52:53], v[142:143]
	v_pk_add_f32 v[138:139], v[50:51], v[138:139]
	v_add_u32_e32 v50, 0xffff4010, v2
	ds_read_b128 v[50:53], v50
	s_waitcnt lgkmcnt(0)
	v_pk_mul_f32 v[142:143], v[124:125], v[50:51] op_sel:[0,1]
	v_pk_mul_f32 v[144:145], v[122:123], v[50:51] op_sel:[0,1]
	v_pk_fma_f32 v[142:143], v[120:121], v[50:51], v[142:143] op_sel_hi:[1,0,1]
	v_pk_fma_f32 v[50:51], v[118:119], v[50:51], v[144:145] op_sel_hi:[1,0,1]
	v_mov_b32_e32 v144, v53
	v_pk_mul_f32 v[146:147], v[112:113], v[144:145] op_sel_hi:[1,0]
	v_pk_mul_f32 v[144:145], v[110:111], v[144:145] op_sel_hi:[1,0]
	v_pk_fma_f32 v[146:147], v[104:105], v[52:53], v[146:147] op_sel_hi:[1,0,1]
	v_pk_fma_f32 v[52:53], v[102:103], v[52:53], v[144:145] op_sel_hi:[1,0,1]
	v_pk_add_f32 v[142:143], v[142:143], v[146:147]
	v_pk_add_f32 v[50:51], v[50:51], v[52:53]
	v_pk_add_f32 v[140:141], v[140:141], v[142:143]
	v_pk_add_f32 v[138:139], v[138:139], v[50:51]
	v_add_u32_e32 v50, 0xffff4020, v2
	ds_read_b128 v[50:53], v50
	s_waitcnt lgkmcnt(0)
	v_pk_mul_f32 v[142:143], v[108:109], v[50:51] op_sel:[0,1]
	v_pk_mul_f32 v[144:145], v[106:107], v[50:51] op_sel:[0,1]
	v_pk_fma_f32 v[142:143], v[100:101], v[50:51], v[142:143] op_sel_hi:[1,0,1]
	v_pk_fma_f32 v[50:51], v[98:99], v[50:51], v[144:145] op_sel_hi:[1,0,1]
	v_mov_b32_e32 v144, v53
	v_pk_mul_f32 v[146:147], v[96:97], v[144:145] op_sel_hi:[1,0]
	v_pk_mul_f32 v[144:145], v[94:95], v[144:145] op_sel_hi:[1,0]
	v_pk_fma_f32 v[146:147], v[84:85], v[52:53], v[146:147] op_sel_hi:[1,0,1]
	v_pk_fma_f32 v[52:53], v[82:83], v[52:53], v[144:145] op_sel_hi:[1,0,1]
	v_pk_add_f32 v[142:143], v[142:143], v[146:147]
	v_pk_add_f32 v[50:51], v[50:51], v[52:53]
	v_pk_add_f32 v[140:141], v[140:141], v[142:143]
	v_pk_add_f32 v[138:139], v[138:139], v[50:51]
	v_add_u32_e32 v50, 0xffff4030, v2
	ds_read_b128 v[50:53], v50
	s_waitcnt lgkmcnt(0)
	v_pk_mul_f32 v[142:143], v[88:89], v[50:51] op_sel:[0,1]
	v_pk_mul_f32 v[144:145], v[86:87], v[50:51] op_sel:[0,1]
	v_pk_fma_f32 v[142:143], v[80:81], v[50:51], v[142:143] op_sel_hi:[1,0,1]
	v_pk_fma_f32 v[50:51], v[78:79], v[50:51], v[144:145] op_sel_hi:[1,0,1]
	v_mov_b32_e32 v144, v53
	v_pk_mul_f32 v[146:147], v[76:77], v[144:145] op_sel_hi:[1,0]
	v_pk_mul_f32 v[144:145], v[74:75], v[144:145] op_sel_hi:[1,0]
	v_pk_fma_f32 v[146:147], v[72:73], v[52:53], v[146:147] op_sel_hi:[1,0,1]
	v_pk_fma_f32 v[52:53], v[70:71], v[52:53], v[144:145] op_sel_hi:[1,0,1]
	v_pk_add_f32 v[142:143], v[142:143], v[146:147]
	v_pk_add_f32 v[50:51], v[50:51], v[52:53]
	v_pk_add_f32 v[52:53], v[140:141], v[142:143]
	v_pk_add_f32 v[50:51], v[138:139], v[50:51]
	v_add_u32_e32 v138, 0xffff5000, v2
	ds_read_b128 v[138:141], v138
	s_waitcnt lgkmcnt(0)
	v_pk_mul_f32 v[142:143], v[136:137], v[138:139] op_sel:[0,1]
	v_pk_mul_f32 v[144:145], v[134:135], v[138:139] op_sel:[0,1]
	v_pk_fma_f32 v[142:143], v[132:133], v[138:139], v[142:143] op_sel_hi:[1,0,1]
	v_pk_fma_f32 v[138:139], v[130:131], v[138:139], v[144:145] op_sel_hi:[1,0,1]
	v_mov_b32_e32 v144, v141
	v_pk_mul_f32 v[146:147], v[128:129], v[144:145] op_sel_hi:[1,0]
	v_pk_mul_f32 v[144:145], v[126:127], v[144:145] op_sel_hi:[1,0]
	v_pk_fma_f32 v[146:147], v[116:117], v[140:141], v[146:147] op_sel_hi:[1,0,1]
	v_pk_fma_f32 v[140:141], v[114:115], v[140:141], v[144:145] op_sel_hi:[1,0,1]
	v_pk_add_f32 v[142:143], v[142:143], v[146:147]
	v_pk_add_f32 v[138:139], v[138:139], v[140:141]
	v_pk_add_f32 v[140:141], v[48:49], v[142:143]
	v_pk_add_f32 v[138:139], v[46:47], v[138:139]
	v_add_u32_e32 v46, 0xffff5010, v2
	ds_read_b128 v[46:49], v46
	s_waitcnt lgkmcnt(0)
	v_pk_mul_f32 v[142:143], v[124:125], v[46:47] op_sel:[0,1]
	v_pk_mul_f32 v[144:145], v[122:123], v[46:47] op_sel:[0,1]
	v_pk_fma_f32 v[142:143], v[120:121], v[46:47], v[142:143] op_sel_hi:[1,0,1]
	v_pk_fma_f32 v[46:47], v[118:119], v[46:47], v[144:145] op_sel_hi:[1,0,1]
	v_mov_b32_e32 v144, v49
	v_pk_mul_f32 v[146:147], v[112:113], v[144:145] op_sel_hi:[1,0]
	v_pk_mul_f32 v[144:145], v[110:111], v[144:145] op_sel_hi:[1,0]
	v_pk_fma_f32 v[146:147], v[104:105], v[48:49], v[146:147] op_sel_hi:[1,0,1]
	v_pk_fma_f32 v[48:49], v[102:103], v[48:49], v[144:145] op_sel_hi:[1,0,1]
	v_pk_add_f32 v[142:143], v[142:143], v[146:147]
	v_pk_add_f32 v[46:47], v[46:47], v[48:49]
	v_pk_add_f32 v[140:141], v[140:141], v[142:143]
	v_pk_add_f32 v[138:139], v[138:139], v[46:47]
	v_add_u32_e32 v46, 0xffff5020, v2
	ds_read_b128 v[46:49], v46
	s_waitcnt lgkmcnt(0)
	v_pk_mul_f32 v[142:143], v[108:109], v[46:47] op_sel:[0,1]
	v_pk_mul_f32 v[144:145], v[106:107], v[46:47] op_sel:[0,1]
	v_pk_fma_f32 v[142:143], v[100:101], v[46:47], v[142:143] op_sel_hi:[1,0,1]
	v_pk_fma_f32 v[46:47], v[98:99], v[46:47], v[144:145] op_sel_hi:[1,0,1]
	v_mov_b32_e32 v144, v49
	v_pk_mul_f32 v[146:147], v[96:97], v[144:145] op_sel_hi:[1,0]
	v_pk_mul_f32 v[144:145], v[94:95], v[144:145] op_sel_hi:[1,0]
	v_pk_fma_f32 v[146:147], v[84:85], v[48:49], v[146:147] op_sel_hi:[1,0,1]
	v_pk_fma_f32 v[48:49], v[82:83], v[48:49], v[144:145] op_sel_hi:[1,0,1]
	v_pk_add_f32 v[142:143], v[142:143], v[146:147]
	v_pk_add_f32 v[46:47], v[46:47], v[48:49]
	v_pk_add_f32 v[140:141], v[140:141], v[142:143]
	v_pk_add_f32 v[138:139], v[138:139], v[46:47]
	v_add_u32_e32 v46, 0xffff5030, v2
	ds_read_b128 v[46:49], v46
	s_waitcnt lgkmcnt(0)
	v_pk_mul_f32 v[142:143], v[88:89], v[46:47] op_sel:[0,1]
	v_pk_mul_f32 v[144:145], v[86:87], v[46:47] op_sel:[0,1]
	v_pk_fma_f32 v[142:143], v[80:81], v[46:47], v[142:143] op_sel_hi:[1,0,1]
	v_pk_fma_f32 v[46:47], v[78:79], v[46:47], v[144:145] op_sel_hi:[1,0,1]
	v_mov_b32_e32 v144, v49
	v_pk_mul_f32 v[146:147], v[76:77], v[144:145] op_sel_hi:[1,0]
	v_pk_mul_f32 v[144:145], v[74:75], v[144:145] op_sel_hi:[1,0]
	v_pk_fma_f32 v[146:147], v[72:73], v[48:49], v[146:147] op_sel_hi:[1,0,1]
	v_pk_fma_f32 v[48:49], v[70:71], v[48:49], v[144:145] op_sel_hi:[1,0,1]
	v_pk_add_f32 v[142:143], v[142:143], v[146:147]
	v_pk_add_f32 v[46:47], v[46:47], v[48:49]
	v_pk_add_f32 v[48:49], v[140:141], v[142:143]
	v_pk_add_f32 v[46:47], v[138:139], v[46:47]
	v_add_u32_e32 v138, 0xffff6000, v2
	ds_read_b128 v[138:141], v138
	s_waitcnt lgkmcnt(0)
	v_pk_mul_f32 v[142:143], v[136:137], v[138:139] op_sel:[0,1]
	v_pk_mul_f32 v[144:145], v[134:135], v[138:139] op_sel:[0,1]
	v_pk_fma_f32 v[142:143], v[132:133], v[138:139], v[142:143] op_sel_hi:[1,0,1]
	v_pk_fma_f32 v[138:139], v[130:131], v[138:139], v[144:145] op_sel_hi:[1,0,1]
	v_mov_b32_e32 v144, v141
	v_pk_mul_f32 v[146:147], v[128:129], v[144:145] op_sel_hi:[1,0]
	v_pk_mul_f32 v[144:145], v[126:127], v[144:145] op_sel_hi:[1,0]
	v_pk_fma_f32 v[146:147], v[116:117], v[140:141], v[146:147] op_sel_hi:[1,0,1]
	v_pk_fma_f32 v[140:141], v[114:115], v[140:141], v[144:145] op_sel_hi:[1,0,1]
	v_pk_add_f32 v[142:143], v[142:143], v[146:147]
	v_pk_add_f32 v[138:139], v[138:139], v[140:141]
	v_pk_add_f32 v[140:141], v[44:45], v[142:143]
	v_pk_add_f32 v[138:139], v[42:43], v[138:139]
	v_add_u32_e32 v42, 0xffff6010, v2
	ds_read_b128 v[42:45], v42
	s_waitcnt lgkmcnt(0)
	v_pk_mul_f32 v[142:143], v[124:125], v[42:43] op_sel:[0,1]
	v_pk_mul_f32 v[144:145], v[122:123], v[42:43] op_sel:[0,1]
	v_pk_fma_f32 v[142:143], v[120:121], v[42:43], v[142:143] op_sel_hi:[1,0,1]
	v_pk_fma_f32 v[42:43], v[118:119], v[42:43], v[144:145] op_sel_hi:[1,0,1]
	v_mov_b32_e32 v144, v45
	v_pk_mul_f32 v[146:147], v[112:113], v[144:145] op_sel_hi:[1,0]
	v_pk_mul_f32 v[144:145], v[110:111], v[144:145] op_sel_hi:[1,0]
	v_pk_fma_f32 v[146:147], v[104:105], v[44:45], v[146:147] op_sel_hi:[1,0,1]
	v_pk_fma_f32 v[44:45], v[102:103], v[44:45], v[144:145] op_sel_hi:[1,0,1]
	v_pk_add_f32 v[142:143], v[142:143], v[146:147]
	v_pk_add_f32 v[42:43], v[42:43], v[44:45]
	v_pk_add_f32 v[140:141], v[140:141], v[142:143]
	v_pk_add_f32 v[138:139], v[138:139], v[42:43]
	v_add_u32_e32 v42, 0xffff6020, v2
	ds_read_b128 v[42:45], v42
	s_waitcnt lgkmcnt(0)
	v_pk_mul_f32 v[142:143], v[108:109], v[42:43] op_sel:[0,1]
	v_pk_mul_f32 v[144:145], v[106:107], v[42:43] op_sel:[0,1]
	v_pk_fma_f32 v[142:143], v[100:101], v[42:43], v[142:143] op_sel_hi:[1,0,1]
	v_pk_fma_f32 v[42:43], v[98:99], v[42:43], v[144:145] op_sel_hi:[1,0,1]
	v_mov_b32_e32 v144, v45
	v_pk_mul_f32 v[146:147], v[96:97], v[144:145] op_sel_hi:[1,0]
	v_pk_mul_f32 v[144:145], v[94:95], v[144:145] op_sel_hi:[1,0]
	v_pk_fma_f32 v[146:147], v[84:85], v[44:45], v[146:147] op_sel_hi:[1,0,1]
	v_pk_fma_f32 v[44:45], v[82:83], v[44:45], v[144:145] op_sel_hi:[1,0,1]
	v_pk_add_f32 v[142:143], v[142:143], v[146:147]
	v_pk_add_f32 v[42:43], v[42:43], v[44:45]
	v_pk_add_f32 v[140:141], v[140:141], v[142:143]
	v_pk_add_f32 v[138:139], v[138:139], v[42:43]
	v_add_u32_e32 v42, 0xffff6030, v2
	ds_read_b128 v[42:45], v42
	s_waitcnt lgkmcnt(0)
	v_pk_mul_f32 v[142:143], v[88:89], v[42:43] op_sel:[0,1]
	v_pk_mul_f32 v[144:145], v[86:87], v[42:43] op_sel:[0,1]
	v_pk_fma_f32 v[142:143], v[80:81], v[42:43], v[142:143] op_sel_hi:[1,0,1]
	v_pk_fma_f32 v[42:43], v[78:79], v[42:43], v[144:145] op_sel_hi:[1,0,1]
	v_mov_b32_e32 v144, v45
	v_pk_mul_f32 v[146:147], v[76:77], v[144:145] op_sel_hi:[1,0]
	v_pk_mul_f32 v[144:145], v[74:75], v[144:145] op_sel_hi:[1,0]
	v_pk_fma_f32 v[146:147], v[72:73], v[44:45], v[146:147] op_sel_hi:[1,0,1]
	v_pk_fma_f32 v[44:45], v[70:71], v[44:45], v[144:145] op_sel_hi:[1,0,1]
	v_pk_add_f32 v[142:143], v[142:143], v[146:147]
	v_pk_add_f32 v[42:43], v[42:43], v[44:45]
	v_pk_add_f32 v[44:45], v[140:141], v[142:143]
	v_pk_add_f32 v[42:43], v[138:139], v[42:43]
	v_add_u32_e32 v138, 0xffff7000, v2
	ds_read_b128 v[138:141], v138
	s_waitcnt lgkmcnt(0)
	v_pk_mul_f32 v[142:143], v[136:137], v[138:139] op_sel:[0,1]
	v_pk_mul_f32 v[144:145], v[134:135], v[138:139] op_sel:[0,1]
	v_pk_fma_f32 v[142:143], v[132:133], v[138:139], v[142:143] op_sel_hi:[1,0,1]
	v_pk_fma_f32 v[138:139], v[130:131], v[138:139], v[144:145] op_sel_hi:[1,0,1]
	v_mov_b32_e32 v144, v141
	v_pk_mul_f32 v[146:147], v[128:129], v[144:145] op_sel_hi:[1,0]
	v_pk_mul_f32 v[144:145], v[126:127], v[144:145] op_sel_hi:[1,0]
	v_pk_fma_f32 v[146:147], v[116:117], v[140:141], v[146:147] op_sel_hi:[1,0,1]
	v_pk_fma_f32 v[140:141], v[114:115], v[140:141], v[144:145] op_sel_hi:[1,0,1]
	v_pk_add_f32 v[142:143], v[142:143], v[146:147]
	v_pk_add_f32 v[138:139], v[138:139], v[140:141]
	v_pk_add_f32 v[140:141], v[40:41], v[142:143]
	v_pk_add_f32 v[138:139], v[38:39], v[138:139]
	v_add_u32_e32 v38, 0xffff7010, v2
	ds_read_b128 v[38:41], v38
	s_waitcnt lgkmcnt(0)
	v_pk_mul_f32 v[142:143], v[124:125], v[38:39] op_sel:[0,1]
	v_pk_mul_f32 v[144:145], v[122:123], v[38:39] op_sel:[0,1]
	v_pk_fma_f32 v[142:143], v[120:121], v[38:39], v[142:143] op_sel_hi:[1,0,1]
	v_pk_fma_f32 v[38:39], v[118:119], v[38:39], v[144:145] op_sel_hi:[1,0,1]
	v_mov_b32_e32 v144, v41
	v_pk_mul_f32 v[146:147], v[112:113], v[144:145] op_sel_hi:[1,0]
	v_pk_mul_f32 v[144:145], v[110:111], v[144:145] op_sel_hi:[1,0]
	v_pk_fma_f32 v[146:147], v[104:105], v[40:41], v[146:147] op_sel_hi:[1,0,1]
	v_pk_fma_f32 v[40:41], v[102:103], v[40:41], v[144:145] op_sel_hi:[1,0,1]
	v_pk_add_f32 v[142:143], v[142:143], v[146:147]
	v_pk_add_f32 v[38:39], v[38:39], v[40:41]
	v_pk_add_f32 v[140:141], v[140:141], v[142:143]
	v_pk_add_f32 v[138:139], v[138:139], v[38:39]
	v_add_u32_e32 v38, 0xffff7020, v2
	ds_read_b128 v[38:41], v38
	s_waitcnt lgkmcnt(0)
	v_pk_mul_f32 v[142:143], v[108:109], v[38:39] op_sel:[0,1]
	v_pk_mul_f32 v[144:145], v[106:107], v[38:39] op_sel:[0,1]
	v_pk_fma_f32 v[142:143], v[100:101], v[38:39], v[142:143] op_sel_hi:[1,0,1]
	v_pk_fma_f32 v[38:39], v[98:99], v[38:39], v[144:145] op_sel_hi:[1,0,1]
	v_mov_b32_e32 v144, v41
	v_pk_mul_f32 v[146:147], v[96:97], v[144:145] op_sel_hi:[1,0]
	v_pk_mul_f32 v[144:145], v[94:95], v[144:145] op_sel_hi:[1,0]
	v_pk_fma_f32 v[146:147], v[84:85], v[40:41], v[146:147] op_sel_hi:[1,0,1]
	v_pk_fma_f32 v[40:41], v[82:83], v[40:41], v[144:145] op_sel_hi:[1,0,1]
	v_pk_add_f32 v[142:143], v[142:143], v[146:147]
	v_pk_add_f32 v[38:39], v[38:39], v[40:41]
	v_pk_add_f32 v[140:141], v[140:141], v[142:143]
	v_pk_add_f32 v[138:139], v[138:139], v[38:39]
	v_add_u32_e32 v38, 0xffff7030, v2
	ds_read_b128 v[38:41], v38
	s_waitcnt lgkmcnt(0)
	v_pk_mul_f32 v[142:143], v[88:89], v[38:39] op_sel:[0,1]
	v_pk_mul_f32 v[144:145], v[86:87], v[38:39] op_sel:[0,1]
	v_pk_fma_f32 v[142:143], v[80:81], v[38:39], v[142:143] op_sel_hi:[1,0,1]
	v_pk_fma_f32 v[38:39], v[78:79], v[38:39], v[144:145] op_sel_hi:[1,0,1]
	v_mov_b32_e32 v144, v41
	v_pk_mul_f32 v[146:147], v[76:77], v[144:145] op_sel_hi:[1,0]
	v_pk_mul_f32 v[144:145], v[74:75], v[144:145] op_sel_hi:[1,0]
	v_pk_fma_f32 v[146:147], v[72:73], v[40:41], v[146:147] op_sel_hi:[1,0,1]
	v_pk_fma_f32 v[40:41], v[70:71], v[40:41], v[144:145] op_sel_hi:[1,0,1]
	v_pk_add_f32 v[142:143], v[142:143], v[146:147]
	v_pk_add_f32 v[38:39], v[38:39], v[40:41]
	v_pk_add_f32 v[40:41], v[140:141], v[142:143]
	v_pk_add_f32 v[38:39], v[138:139], v[38:39]
	v_add_u32_e32 v138, 0xffff8000, v2
	ds_read_b128 v[138:141], v138
	s_waitcnt lgkmcnt(0)
	v_pk_mul_f32 v[142:143], v[136:137], v[138:139] op_sel:[0,1]
	v_pk_mul_f32 v[144:145], v[134:135], v[138:139] op_sel:[0,1]
	v_pk_fma_f32 v[142:143], v[132:133], v[138:139], v[142:143] op_sel_hi:[1,0,1]
	v_pk_fma_f32 v[138:139], v[130:131], v[138:139], v[144:145] op_sel_hi:[1,0,1]
	v_mov_b32_e32 v144, v141
	v_pk_mul_f32 v[146:147], v[128:129], v[144:145] op_sel_hi:[1,0]
	v_pk_mul_f32 v[144:145], v[126:127], v[144:145] op_sel_hi:[1,0]
	v_pk_fma_f32 v[146:147], v[116:117], v[140:141], v[146:147] op_sel_hi:[1,0,1]
	v_pk_fma_f32 v[140:141], v[114:115], v[140:141], v[144:145] op_sel_hi:[1,0,1]
	v_pk_add_f32 v[142:143], v[142:143], v[146:147]
	v_pk_add_f32 v[138:139], v[138:139], v[140:141]
	v_pk_add_f32 v[140:141], v[36:37], v[142:143]
	v_pk_add_f32 v[138:139], v[34:35], v[138:139]
	v_add_u32_e32 v34, 0xffff8010, v2
	ds_read_b128 v[34:37], v34
	s_waitcnt lgkmcnt(0)
	v_pk_mul_f32 v[142:143], v[124:125], v[34:35] op_sel:[0,1]
	v_pk_mul_f32 v[144:145], v[122:123], v[34:35] op_sel:[0,1]
	v_pk_fma_f32 v[142:143], v[120:121], v[34:35], v[142:143] op_sel_hi:[1,0,1]
	v_pk_fma_f32 v[34:35], v[118:119], v[34:35], v[144:145] op_sel_hi:[1,0,1]
	v_mov_b32_e32 v144, v37
	v_pk_mul_f32 v[146:147], v[112:113], v[144:145] op_sel_hi:[1,0]
	v_pk_mul_f32 v[144:145], v[110:111], v[144:145] op_sel_hi:[1,0]
	v_pk_fma_f32 v[146:147], v[104:105], v[36:37], v[146:147] op_sel_hi:[1,0,1]
	v_pk_fma_f32 v[36:37], v[102:103], v[36:37], v[144:145] op_sel_hi:[1,0,1]
	v_pk_add_f32 v[142:143], v[142:143], v[146:147]
	v_pk_add_f32 v[34:35], v[34:35], v[36:37]
	v_pk_add_f32 v[140:141], v[140:141], v[142:143]
	v_pk_add_f32 v[138:139], v[138:139], v[34:35]
	v_add_u32_e32 v34, 0xffff8020, v2
	ds_read_b128 v[34:37], v34
	s_waitcnt lgkmcnt(0)
	v_pk_mul_f32 v[142:143], v[108:109], v[34:35] op_sel:[0,1]
	v_pk_mul_f32 v[144:145], v[106:107], v[34:35] op_sel:[0,1]
	v_pk_fma_f32 v[142:143], v[100:101], v[34:35], v[142:143] op_sel_hi:[1,0,1]
	v_pk_fma_f32 v[34:35], v[98:99], v[34:35], v[144:145] op_sel_hi:[1,0,1]
	v_mov_b32_e32 v144, v37
	v_pk_mul_f32 v[146:147], v[96:97], v[144:145] op_sel_hi:[1,0]
	v_pk_mul_f32 v[144:145], v[94:95], v[144:145] op_sel_hi:[1,0]
	v_pk_fma_f32 v[146:147], v[84:85], v[36:37], v[146:147] op_sel_hi:[1,0,1]
	v_pk_fma_f32 v[36:37], v[82:83], v[36:37], v[144:145] op_sel_hi:[1,0,1]
	v_pk_add_f32 v[142:143], v[142:143], v[146:147]
	v_pk_add_f32 v[34:35], v[34:35], v[36:37]
	v_pk_add_f32 v[140:141], v[140:141], v[142:143]
	v_pk_add_f32 v[138:139], v[138:139], v[34:35]
	v_add_u32_e32 v34, 0xffff8030, v2
	ds_read_b128 v[34:37], v34
	s_waitcnt lgkmcnt(0)
	v_pk_mul_f32 v[142:143], v[88:89], v[34:35] op_sel:[0,1]
	v_pk_mul_f32 v[144:145], v[86:87], v[34:35] op_sel:[0,1]
	v_pk_fma_f32 v[142:143], v[80:81], v[34:35], v[142:143] op_sel_hi:[1,0,1]
	v_pk_fma_f32 v[34:35], v[78:79], v[34:35], v[144:145] op_sel_hi:[1,0,1]
	v_mov_b32_e32 v144, v37
	v_pk_mul_f32 v[146:147], v[76:77], v[144:145] op_sel_hi:[1,0]
	v_pk_mul_f32 v[144:145], v[74:75], v[144:145] op_sel_hi:[1,0]
	v_pk_fma_f32 v[146:147], v[72:73], v[36:37], v[146:147] op_sel_hi:[1,0,1]
	v_pk_fma_f32 v[36:37], v[70:71], v[36:37], v[144:145] op_sel_hi:[1,0,1]
	v_pk_add_f32 v[142:143], v[142:143], v[146:147]
	v_pk_add_f32 v[34:35], v[34:35], v[36:37]
	v_pk_add_f32 v[36:37], v[140:141], v[142:143]
	v_pk_add_f32 v[34:35], v[138:139], v[34:35]
	v_add_u32_e32 v138, 0xffff9000, v2
	ds_read_b128 v[138:141], v138
	s_waitcnt lgkmcnt(0)
	v_pk_mul_f32 v[142:143], v[136:137], v[138:139] op_sel:[0,1]
	v_pk_mul_f32 v[144:145], v[134:135], v[138:139] op_sel:[0,1]
	v_pk_fma_f32 v[142:143], v[132:133], v[138:139], v[142:143] op_sel_hi:[1,0,1]
	v_pk_fma_f32 v[138:139], v[130:131], v[138:139], v[144:145] op_sel_hi:[1,0,1]
	v_mov_b32_e32 v144, v141
	v_pk_mul_f32 v[146:147], v[128:129], v[144:145] op_sel_hi:[1,0]
	v_pk_mul_f32 v[144:145], v[126:127], v[144:145] op_sel_hi:[1,0]
	v_pk_fma_f32 v[146:147], v[116:117], v[140:141], v[146:147] op_sel_hi:[1,0,1]
	v_pk_fma_f32 v[140:141], v[114:115], v[140:141], v[144:145] op_sel_hi:[1,0,1]
	v_pk_add_f32 v[142:143], v[142:143], v[146:147]
	v_pk_add_f32 v[138:139], v[138:139], v[140:141]
	v_pk_add_f32 v[140:141], v[32:33], v[142:143]
	v_pk_add_f32 v[138:139], v[30:31], v[138:139]
	v_add_u32_e32 v30, 0xffff9010, v2
	ds_read_b128 v[30:33], v30
	s_waitcnt lgkmcnt(0)
	v_pk_mul_f32 v[142:143], v[124:125], v[30:31] op_sel:[0,1]
	v_pk_mul_f32 v[144:145], v[122:123], v[30:31] op_sel:[0,1]
	v_pk_fma_f32 v[142:143], v[120:121], v[30:31], v[142:143] op_sel_hi:[1,0,1]
	v_pk_fma_f32 v[30:31], v[118:119], v[30:31], v[144:145] op_sel_hi:[1,0,1]
	v_mov_b32_e32 v144, v33
	v_pk_mul_f32 v[146:147], v[112:113], v[144:145] op_sel_hi:[1,0]
	v_pk_mul_f32 v[144:145], v[110:111], v[144:145] op_sel_hi:[1,0]
	v_pk_fma_f32 v[146:147], v[104:105], v[32:33], v[146:147] op_sel_hi:[1,0,1]
	v_pk_fma_f32 v[32:33], v[102:103], v[32:33], v[144:145] op_sel_hi:[1,0,1]
	v_pk_add_f32 v[142:143], v[142:143], v[146:147]
	v_pk_add_f32 v[30:31], v[30:31], v[32:33]
	v_pk_add_f32 v[140:141], v[140:141], v[142:143]
	v_pk_add_f32 v[138:139], v[138:139], v[30:31]
	v_add_u32_e32 v30, 0xffff9020, v2
	ds_read_b128 v[30:33], v30
	s_waitcnt lgkmcnt(0)
	v_pk_mul_f32 v[142:143], v[108:109], v[30:31] op_sel:[0,1]
	v_pk_mul_f32 v[144:145], v[106:107], v[30:31] op_sel:[0,1]
	v_pk_fma_f32 v[142:143], v[100:101], v[30:31], v[142:143] op_sel_hi:[1,0,1]
	v_pk_fma_f32 v[30:31], v[98:99], v[30:31], v[144:145] op_sel_hi:[1,0,1]
	v_mov_b32_e32 v144, v33
	v_pk_mul_f32 v[146:147], v[96:97], v[144:145] op_sel_hi:[1,0]
	v_pk_mul_f32 v[144:145], v[94:95], v[144:145] op_sel_hi:[1,0]
	v_pk_fma_f32 v[146:147], v[84:85], v[32:33], v[146:147] op_sel_hi:[1,0,1]
	v_pk_fma_f32 v[32:33], v[82:83], v[32:33], v[144:145] op_sel_hi:[1,0,1]
	v_pk_add_f32 v[142:143], v[142:143], v[146:147]
	v_pk_add_f32 v[30:31], v[30:31], v[32:33]
	v_pk_add_f32 v[140:141], v[140:141], v[142:143]
	v_pk_add_f32 v[138:139], v[138:139], v[30:31]
	v_add_u32_e32 v30, 0xffff9030, v2
	ds_read_b128 v[30:33], v30
	s_waitcnt lgkmcnt(0)
	v_pk_mul_f32 v[142:143], v[88:89], v[30:31] op_sel:[0,1]
	v_pk_mul_f32 v[144:145], v[86:87], v[30:31] op_sel:[0,1]
	v_pk_fma_f32 v[142:143], v[80:81], v[30:31], v[142:143] op_sel_hi:[1,0,1]
	v_pk_fma_f32 v[30:31], v[78:79], v[30:31], v[144:145] op_sel_hi:[1,0,1]
	v_mov_b32_e32 v144, v33
	v_pk_mul_f32 v[146:147], v[76:77], v[144:145] op_sel_hi:[1,0]
	v_pk_mul_f32 v[144:145], v[74:75], v[144:145] op_sel_hi:[1,0]
	v_pk_fma_f32 v[146:147], v[72:73], v[32:33], v[146:147] op_sel_hi:[1,0,1]
	v_pk_fma_f32 v[32:33], v[70:71], v[32:33], v[144:145] op_sel_hi:[1,0,1]
	v_pk_add_f32 v[142:143], v[142:143], v[146:147]
	v_pk_add_f32 v[30:31], v[30:31], v[32:33]
	v_pk_add_f32 v[32:33], v[140:141], v[142:143]
	v_pk_add_f32 v[30:31], v[138:139], v[30:31]
	v_add_u32_e32 v138, 0xffffa000, v2
	ds_read_b128 v[138:141], v138
	s_waitcnt lgkmcnt(0)
	v_pk_mul_f32 v[142:143], v[136:137], v[138:139] op_sel:[0,1]
	v_pk_mul_f32 v[144:145], v[134:135], v[138:139] op_sel:[0,1]
	v_pk_fma_f32 v[142:143], v[132:133], v[138:139], v[142:143] op_sel_hi:[1,0,1]
	v_pk_fma_f32 v[138:139], v[130:131], v[138:139], v[144:145] op_sel_hi:[1,0,1]
	v_mov_b32_e32 v144, v141
	v_pk_mul_f32 v[146:147], v[128:129], v[144:145] op_sel_hi:[1,0]
	v_pk_mul_f32 v[144:145], v[126:127], v[144:145] op_sel_hi:[1,0]
	v_pk_fma_f32 v[146:147], v[116:117], v[140:141], v[146:147] op_sel_hi:[1,0,1]
	v_pk_fma_f32 v[140:141], v[114:115], v[140:141], v[144:145] op_sel_hi:[1,0,1]
	v_pk_add_f32 v[142:143], v[142:143], v[146:147]
	v_pk_add_f32 v[138:139], v[138:139], v[140:141]
	v_pk_add_f32 v[140:141], v[28:29], v[142:143]
	v_pk_add_f32 v[138:139], v[26:27], v[138:139]
	v_add_u32_e32 v26, 0xffffa010, v2
	ds_read_b128 v[26:29], v26
	s_waitcnt lgkmcnt(0)
	v_pk_mul_f32 v[142:143], v[124:125], v[26:27] op_sel:[0,1]
	v_pk_mul_f32 v[144:145], v[122:123], v[26:27] op_sel:[0,1]
	v_pk_fma_f32 v[142:143], v[120:121], v[26:27], v[142:143] op_sel_hi:[1,0,1]
	v_pk_fma_f32 v[26:27], v[118:119], v[26:27], v[144:145] op_sel_hi:[1,0,1]
	v_mov_b32_e32 v144, v29
	v_pk_mul_f32 v[146:147], v[112:113], v[144:145] op_sel_hi:[1,0]
	v_pk_mul_f32 v[144:145], v[110:111], v[144:145] op_sel_hi:[1,0]
	v_pk_fma_f32 v[146:147], v[104:105], v[28:29], v[146:147] op_sel_hi:[1,0,1]
	v_pk_fma_f32 v[28:29], v[102:103], v[28:29], v[144:145] op_sel_hi:[1,0,1]
	v_pk_add_f32 v[142:143], v[142:143], v[146:147]
	v_pk_add_f32 v[26:27], v[26:27], v[28:29]
	v_pk_add_f32 v[140:141], v[140:141], v[142:143]
	v_pk_add_f32 v[138:139], v[138:139], v[26:27]
	v_add_u32_e32 v26, 0xffffa020, v2
	ds_read_b128 v[26:29], v26
	s_waitcnt lgkmcnt(0)
	v_pk_mul_f32 v[142:143], v[108:109], v[26:27] op_sel:[0,1]
	v_pk_mul_f32 v[144:145], v[106:107], v[26:27] op_sel:[0,1]
	v_pk_fma_f32 v[142:143], v[100:101], v[26:27], v[142:143] op_sel_hi:[1,0,1]
	v_pk_fma_f32 v[26:27], v[98:99], v[26:27], v[144:145] op_sel_hi:[1,0,1]
	v_mov_b32_e32 v144, v29
	v_pk_mul_f32 v[146:147], v[96:97], v[144:145] op_sel_hi:[1,0]
	v_pk_mul_f32 v[144:145], v[94:95], v[144:145] op_sel_hi:[1,0]
	v_pk_fma_f32 v[146:147], v[84:85], v[28:29], v[146:147] op_sel_hi:[1,0,1]
	v_pk_fma_f32 v[28:29], v[82:83], v[28:29], v[144:145] op_sel_hi:[1,0,1]
	v_pk_add_f32 v[142:143], v[142:143], v[146:147]
	v_pk_add_f32 v[26:27], v[26:27], v[28:29]
	v_pk_add_f32 v[140:141], v[140:141], v[142:143]
	v_pk_add_f32 v[138:139], v[138:139], v[26:27]
	v_add_u32_e32 v26, 0xffffa030, v2
	ds_read_b128 v[26:29], v26
	s_waitcnt lgkmcnt(0)
	v_pk_mul_f32 v[142:143], v[88:89], v[26:27] op_sel:[0,1]
	v_pk_mul_f32 v[144:145], v[86:87], v[26:27] op_sel:[0,1]
	v_pk_fma_f32 v[142:143], v[80:81], v[26:27], v[142:143] op_sel_hi:[1,0,1]
	v_pk_fma_f32 v[26:27], v[78:79], v[26:27], v[144:145] op_sel_hi:[1,0,1]
	v_mov_b32_e32 v144, v29
	v_pk_mul_f32 v[146:147], v[76:77], v[144:145] op_sel_hi:[1,0]
	v_pk_mul_f32 v[144:145], v[74:75], v[144:145] op_sel_hi:[1,0]
	v_pk_fma_f32 v[146:147], v[72:73], v[28:29], v[146:147] op_sel_hi:[1,0,1]
	v_pk_fma_f32 v[28:29], v[70:71], v[28:29], v[144:145] op_sel_hi:[1,0,1]
	v_pk_add_f32 v[142:143], v[142:143], v[146:147]
	v_pk_add_f32 v[26:27], v[26:27], v[28:29]
	v_pk_add_f32 v[28:29], v[140:141], v[142:143]
	v_pk_add_f32 v[26:27], v[138:139], v[26:27]
	v_add_u32_e32 v138, 0xffffb000, v2
	ds_read_b128 v[138:141], v138
	s_waitcnt lgkmcnt(0)
	v_pk_mul_f32 v[142:143], v[136:137], v[138:139] op_sel:[0,1]
	v_pk_mul_f32 v[144:145], v[134:135], v[138:139] op_sel:[0,1]
	v_pk_fma_f32 v[142:143], v[132:133], v[138:139], v[142:143] op_sel_hi:[1,0,1]
	v_pk_fma_f32 v[138:139], v[130:131], v[138:139], v[144:145] op_sel_hi:[1,0,1]
	v_mov_b32_e32 v144, v141
	v_pk_mul_f32 v[146:147], v[128:129], v[144:145] op_sel_hi:[1,0]
	v_pk_mul_f32 v[144:145], v[126:127], v[144:145] op_sel_hi:[1,0]
	v_pk_fma_f32 v[146:147], v[116:117], v[140:141], v[146:147] op_sel_hi:[1,0,1]
	v_pk_fma_f32 v[140:141], v[114:115], v[140:141], v[144:145] op_sel_hi:[1,0,1]
	v_pk_add_f32 v[142:143], v[142:143], v[146:147]
	v_pk_add_f32 v[138:139], v[138:139], v[140:141]
	v_pk_add_f32 v[140:141], v[20:21], v[142:143]
	v_pk_add_f32 v[138:139], v[18:19], v[138:139]
	v_add_u32_e32 v18, 0xffffb010, v2
	ds_read_b128 v[18:21], v18
	s_waitcnt lgkmcnt(0)
	v_pk_mul_f32 v[142:143], v[124:125], v[18:19] op_sel:[0,1]
	v_pk_mul_f32 v[144:145], v[122:123], v[18:19] op_sel:[0,1]
	v_pk_fma_f32 v[142:143], v[120:121], v[18:19], v[142:143] op_sel_hi:[1,0,1]
	v_pk_fma_f32 v[18:19], v[118:119], v[18:19], v[144:145] op_sel_hi:[1,0,1]
	v_mov_b32_e32 v144, v21
	v_pk_mul_f32 v[146:147], v[112:113], v[144:145] op_sel_hi:[1,0]
	v_pk_mul_f32 v[144:145], v[110:111], v[144:145] op_sel_hi:[1,0]
	v_pk_fma_f32 v[146:147], v[104:105], v[20:21], v[146:147] op_sel_hi:[1,0,1]
	v_pk_fma_f32 v[20:21], v[102:103], v[20:21], v[144:145] op_sel_hi:[1,0,1]
	v_pk_add_f32 v[142:143], v[142:143], v[146:147]
	v_pk_add_f32 v[18:19], v[18:19], v[20:21]
	v_pk_add_f32 v[140:141], v[140:141], v[142:143]
	v_pk_add_f32 v[138:139], v[138:139], v[18:19]
	v_add_u32_e32 v18, 0xffffb020, v2
	ds_read_b128 v[18:21], v18
	s_waitcnt lgkmcnt(0)
	v_pk_mul_f32 v[142:143], v[108:109], v[18:19] op_sel:[0,1]
	v_pk_mul_f32 v[144:145], v[106:107], v[18:19] op_sel:[0,1]
	v_pk_fma_f32 v[142:143], v[100:101], v[18:19], v[142:143] op_sel_hi:[1,0,1]
	v_pk_fma_f32 v[18:19], v[98:99], v[18:19], v[144:145] op_sel_hi:[1,0,1]
	v_mov_b32_e32 v144, v21
	v_pk_mul_f32 v[146:147], v[96:97], v[144:145] op_sel_hi:[1,0]
	v_pk_mul_f32 v[144:145], v[94:95], v[144:145] op_sel_hi:[1,0]
	v_pk_fma_f32 v[146:147], v[84:85], v[20:21], v[146:147] op_sel_hi:[1,0,1]
	v_pk_fma_f32 v[20:21], v[82:83], v[20:21], v[144:145] op_sel_hi:[1,0,1]
	v_pk_add_f32 v[142:143], v[142:143], v[146:147]
	v_pk_add_f32 v[18:19], v[18:19], v[20:21]
	v_pk_add_f32 v[140:141], v[140:141], v[142:143]
	v_pk_add_f32 v[138:139], v[138:139], v[18:19]
	v_add_u32_e32 v18, 0xffffb030, v2
	ds_read_b128 v[18:21], v18
	s_waitcnt lgkmcnt(0)
	v_pk_mul_f32 v[142:143], v[88:89], v[18:19] op_sel:[0,1]
	v_pk_mul_f32 v[144:145], v[86:87], v[18:19] op_sel:[0,1]
	v_pk_fma_f32 v[142:143], v[80:81], v[18:19], v[142:143] op_sel_hi:[1,0,1]
	v_pk_fma_f32 v[18:19], v[78:79], v[18:19], v[144:145] op_sel_hi:[1,0,1]
	v_mov_b32_e32 v144, v21
	v_pk_mul_f32 v[146:147], v[76:77], v[144:145] op_sel_hi:[1,0]
	v_pk_mul_f32 v[144:145], v[74:75], v[144:145] op_sel_hi:[1,0]
	v_pk_fma_f32 v[146:147], v[72:73], v[20:21], v[146:147] op_sel_hi:[1,0,1]
	v_pk_fma_f32 v[20:21], v[70:71], v[20:21], v[144:145] op_sel_hi:[1,0,1]
	v_pk_add_f32 v[142:143], v[142:143], v[146:147]
	v_pk_add_f32 v[18:19], v[18:19], v[20:21]
	v_pk_add_f32 v[20:21], v[140:141], v[142:143]
	v_pk_add_f32 v[18:19], v[138:139], v[18:19]
	v_add_u32_e32 v138, 0xffffc000, v2
	ds_read_b128 v[138:141], v138
	s_waitcnt lgkmcnt(0)
	v_pk_mul_f32 v[142:143], v[136:137], v[138:139] op_sel:[0,1]
	v_pk_mul_f32 v[144:145], v[134:135], v[138:139] op_sel:[0,1]
	v_pk_fma_f32 v[142:143], v[132:133], v[138:139], v[142:143] op_sel_hi:[1,0,1]
	v_pk_fma_f32 v[138:139], v[130:131], v[138:139], v[144:145] op_sel_hi:[1,0,1]
	v_mov_b32_e32 v144, v141
	v_pk_mul_f32 v[146:147], v[128:129], v[144:145] op_sel_hi:[1,0]
	v_pk_mul_f32 v[144:145], v[126:127], v[144:145] op_sel_hi:[1,0]
	v_pk_fma_f32 v[146:147], v[116:117], v[140:141], v[146:147] op_sel_hi:[1,0,1]
	v_pk_fma_f32 v[140:141], v[114:115], v[140:141], v[144:145] op_sel_hi:[1,0,1]
	v_pk_add_f32 v[142:143], v[142:143], v[146:147]
	v_pk_add_f32 v[138:139], v[138:139], v[140:141]
	v_pk_add_f32 v[140:141], v[16:17], v[142:143]
	v_pk_add_f32 v[138:139], v[14:15], v[138:139]
	v_add_u32_e32 v14, 0xffffc010, v2
	ds_read_b128 v[14:17], v14
	s_waitcnt lgkmcnt(0)
	v_pk_mul_f32 v[142:143], v[124:125], v[14:15] op_sel:[0,1]
	v_pk_mul_f32 v[144:145], v[122:123], v[14:15] op_sel:[0,1]
	v_pk_fma_f32 v[142:143], v[120:121], v[14:15], v[142:143] op_sel_hi:[1,0,1]
	v_pk_fma_f32 v[14:15], v[118:119], v[14:15], v[144:145] op_sel_hi:[1,0,1]
	v_mov_b32_e32 v144, v17
	v_pk_mul_f32 v[146:147], v[112:113], v[144:145] op_sel_hi:[1,0]
	v_pk_mul_f32 v[144:145], v[110:111], v[144:145] op_sel_hi:[1,0]
	v_pk_fma_f32 v[146:147], v[104:105], v[16:17], v[146:147] op_sel_hi:[1,0,1]
	v_pk_fma_f32 v[16:17], v[102:103], v[16:17], v[144:145] op_sel_hi:[1,0,1]
	v_pk_add_f32 v[142:143], v[142:143], v[146:147]
	v_pk_add_f32 v[14:15], v[14:15], v[16:17]
	v_pk_add_f32 v[140:141], v[140:141], v[142:143]
	v_pk_add_f32 v[138:139], v[138:139], v[14:15]
	v_add_u32_e32 v14, 0xffffc020, v2
	ds_read_b128 v[14:17], v14
	s_waitcnt lgkmcnt(0)
	v_pk_mul_f32 v[142:143], v[108:109], v[14:15] op_sel:[0,1]
	v_pk_mul_f32 v[144:145], v[106:107], v[14:15] op_sel:[0,1]
	v_pk_fma_f32 v[142:143], v[100:101], v[14:15], v[142:143] op_sel_hi:[1,0,1]
	v_pk_fma_f32 v[14:15], v[98:99], v[14:15], v[144:145] op_sel_hi:[1,0,1]
	v_mov_b32_e32 v144, v17
	v_pk_mul_f32 v[146:147], v[96:97], v[144:145] op_sel_hi:[1,0]
	v_pk_mul_f32 v[144:145], v[94:95], v[144:145] op_sel_hi:[1,0]
	v_pk_fma_f32 v[146:147], v[84:85], v[16:17], v[146:147] op_sel_hi:[1,0,1]
	v_pk_fma_f32 v[16:17], v[82:83], v[16:17], v[144:145] op_sel_hi:[1,0,1]
	v_pk_add_f32 v[142:143], v[142:143], v[146:147]
	v_pk_add_f32 v[14:15], v[14:15], v[16:17]
	v_pk_add_f32 v[140:141], v[140:141], v[142:143]
	v_pk_add_f32 v[138:139], v[138:139], v[14:15]
	v_add_u32_e32 v14, 0xffffc030, v2
	ds_read_b128 v[14:17], v14
	s_waitcnt lgkmcnt(0)
	v_pk_mul_f32 v[142:143], v[88:89], v[14:15] op_sel:[0,1]
	v_pk_mul_f32 v[144:145], v[86:87], v[14:15] op_sel:[0,1]
	v_pk_fma_f32 v[142:143], v[80:81], v[14:15], v[142:143] op_sel_hi:[1,0,1]
	v_pk_fma_f32 v[14:15], v[78:79], v[14:15], v[144:145] op_sel_hi:[1,0,1]
	v_mov_b32_e32 v144, v17
	v_pk_mul_f32 v[146:147], v[76:77], v[144:145] op_sel_hi:[1,0]
	v_pk_mul_f32 v[144:145], v[74:75], v[144:145] op_sel_hi:[1,0]
	v_pk_fma_f32 v[146:147], v[72:73], v[16:17], v[146:147] op_sel_hi:[1,0,1]
	v_pk_fma_f32 v[16:17], v[70:71], v[16:17], v[144:145] op_sel_hi:[1,0,1]
	v_pk_add_f32 v[142:143], v[142:143], v[146:147]
	v_pk_add_f32 v[14:15], v[14:15], v[16:17]
	v_pk_add_f32 v[16:17], v[140:141], v[142:143]
	v_pk_add_f32 v[14:15], v[138:139], v[14:15]
	v_add_u32_e32 v138, 0xffffd000, v2
	ds_read_b128 v[138:141], v138
	s_waitcnt lgkmcnt(0)
	v_pk_mul_f32 v[142:143], v[136:137], v[138:139] op_sel:[0,1]
	v_pk_mul_f32 v[144:145], v[134:135], v[138:139] op_sel:[0,1]
	v_pk_fma_f32 v[142:143], v[132:133], v[138:139], v[142:143] op_sel_hi:[1,0,1]
	v_pk_fma_f32 v[138:139], v[130:131], v[138:139], v[144:145] op_sel_hi:[1,0,1]
	v_mov_b32_e32 v144, v141
	v_pk_mul_f32 v[146:147], v[128:129], v[144:145] op_sel_hi:[1,0]
	v_pk_mul_f32 v[144:145], v[126:127], v[144:145] op_sel_hi:[1,0]
	v_pk_fma_f32 v[146:147], v[116:117], v[140:141], v[146:147] op_sel_hi:[1,0,1]
	v_pk_fma_f32 v[140:141], v[114:115], v[140:141], v[144:145] op_sel_hi:[1,0,1]
	v_pk_add_f32 v[142:143], v[142:143], v[146:147]
	v_pk_add_f32 v[138:139], v[138:139], v[140:141]
	v_pk_add_f32 v[140:141], v[12:13], v[142:143]
	v_pk_add_f32 v[138:139], v[10:11], v[138:139]
	v_add_u32_e32 v10, 0xffffd010, v2
	ds_read_b128 v[10:13], v10
	s_waitcnt lgkmcnt(0)
	v_pk_mul_f32 v[142:143], v[124:125], v[10:11] op_sel:[0,1]
	v_pk_mul_f32 v[144:145], v[122:123], v[10:11] op_sel:[0,1]
	v_pk_fma_f32 v[142:143], v[120:121], v[10:11], v[142:143] op_sel_hi:[1,0,1]
	v_pk_fma_f32 v[10:11], v[118:119], v[10:11], v[144:145] op_sel_hi:[1,0,1]
	v_mov_b32_e32 v144, v13
	v_pk_mul_f32 v[146:147], v[112:113], v[144:145] op_sel_hi:[1,0]
	v_pk_mul_f32 v[144:145], v[110:111], v[144:145] op_sel_hi:[1,0]
	v_pk_fma_f32 v[146:147], v[104:105], v[12:13], v[146:147] op_sel_hi:[1,0,1]
	v_pk_fma_f32 v[12:13], v[102:103], v[12:13], v[144:145] op_sel_hi:[1,0,1]
	v_pk_add_f32 v[142:143], v[142:143], v[146:147]
	v_pk_add_f32 v[10:11], v[10:11], v[12:13]
	v_pk_add_f32 v[140:141], v[140:141], v[142:143]
	v_pk_add_f32 v[138:139], v[138:139], v[10:11]
	v_add_u32_e32 v10, 0xffffd020, v2
	ds_read_b128 v[10:13], v10
	s_waitcnt lgkmcnt(0)
	v_pk_mul_f32 v[142:143], v[108:109], v[10:11] op_sel:[0,1]
	v_pk_mul_f32 v[144:145], v[106:107], v[10:11] op_sel:[0,1]
	v_pk_fma_f32 v[142:143], v[100:101], v[10:11], v[142:143] op_sel_hi:[1,0,1]
	v_pk_fma_f32 v[10:11], v[98:99], v[10:11], v[144:145] op_sel_hi:[1,0,1]
	v_mov_b32_e32 v144, v13
	v_pk_mul_f32 v[146:147], v[96:97], v[144:145] op_sel_hi:[1,0]
	v_pk_mul_f32 v[144:145], v[94:95], v[144:145] op_sel_hi:[1,0]
	v_pk_fma_f32 v[146:147], v[84:85], v[12:13], v[146:147] op_sel_hi:[1,0,1]
	v_pk_fma_f32 v[12:13], v[82:83], v[12:13], v[144:145] op_sel_hi:[1,0,1]
	v_pk_add_f32 v[142:143], v[142:143], v[146:147]
	v_pk_add_f32 v[10:11], v[10:11], v[12:13]
	v_pk_add_f32 v[140:141], v[140:141], v[142:143]
	v_pk_add_f32 v[138:139], v[138:139], v[10:11]
	v_add_u32_e32 v10, 0xffffd030, v2
	ds_read_b128 v[10:13], v10
	s_waitcnt lgkmcnt(0)
	v_pk_mul_f32 v[142:143], v[88:89], v[10:11] op_sel:[0,1]
	v_pk_mul_f32 v[144:145], v[86:87], v[10:11] op_sel:[0,1]
	v_pk_fma_f32 v[142:143], v[80:81], v[10:11], v[142:143] op_sel_hi:[1,0,1]
	v_pk_fma_f32 v[10:11], v[78:79], v[10:11], v[144:145] op_sel_hi:[1,0,1]
	v_mov_b32_e32 v144, v13
	v_pk_mul_f32 v[146:147], v[76:77], v[144:145] op_sel_hi:[1,0]
	v_pk_mul_f32 v[144:145], v[74:75], v[144:145] op_sel_hi:[1,0]
	v_pk_fma_f32 v[146:147], v[72:73], v[12:13], v[146:147] op_sel_hi:[1,0,1]
	v_pk_fma_f32 v[12:13], v[70:71], v[12:13], v[144:145] op_sel_hi:[1,0,1]
	v_pk_add_f32 v[142:143], v[142:143], v[146:147]
	v_pk_add_f32 v[10:11], v[10:11], v[12:13]
	v_pk_add_f32 v[12:13], v[140:141], v[142:143]
	v_pk_add_f32 v[10:11], v[138:139], v[10:11]
	v_add_u32_e32 v138, 0xffffe000, v2
	ds_read_b128 v[138:141], v138
	s_waitcnt lgkmcnt(0)
	v_pk_mul_f32 v[142:143], v[136:137], v[138:139] op_sel:[0,1]
	v_pk_mul_f32 v[144:145], v[134:135], v[138:139] op_sel:[0,1]
	v_pk_fma_f32 v[142:143], v[132:133], v[138:139], v[142:143] op_sel_hi:[1,0,1]
	v_pk_fma_f32 v[138:139], v[130:131], v[138:139], v[144:145] op_sel_hi:[1,0,1]
	v_mov_b32_e32 v144, v141
	v_pk_mul_f32 v[146:147], v[128:129], v[144:145] op_sel_hi:[1,0]
	v_pk_mul_f32 v[144:145], v[126:127], v[144:145] op_sel_hi:[1,0]
	v_pk_fma_f32 v[146:147], v[116:117], v[140:141], v[146:147] op_sel_hi:[1,0,1]
	v_pk_fma_f32 v[140:141], v[114:115], v[140:141], v[144:145] op_sel_hi:[1,0,1]
	v_pk_add_f32 v[142:143], v[142:143], v[146:147]
	v_pk_add_f32 v[138:139], v[138:139], v[140:141]
	v_pk_add_f32 v[140:141], v[24:25], v[142:143]
	v_pk_add_f32 v[138:139], v[22:23], v[138:139]
	v_add_u32_e32 v22, 0xffffe010, v2
	ds_read_b128 v[22:25], v22
	s_waitcnt lgkmcnt(0)
	v_pk_mul_f32 v[142:143], v[124:125], v[22:23] op_sel:[0,1]
	v_pk_mul_f32 v[144:145], v[122:123], v[22:23] op_sel:[0,1]
	v_pk_fma_f32 v[142:143], v[120:121], v[22:23], v[142:143] op_sel_hi:[1,0,1]
	v_pk_fma_f32 v[22:23], v[118:119], v[22:23], v[144:145] op_sel_hi:[1,0,1]
	v_mov_b32_e32 v144, v25
	v_pk_mul_f32 v[146:147], v[112:113], v[144:145] op_sel_hi:[1,0]
	v_pk_mul_f32 v[144:145], v[110:111], v[144:145] op_sel_hi:[1,0]
	v_pk_fma_f32 v[146:147], v[104:105], v[24:25], v[146:147] op_sel_hi:[1,0,1]
	v_pk_fma_f32 v[24:25], v[102:103], v[24:25], v[144:145] op_sel_hi:[1,0,1]
	v_pk_add_f32 v[142:143], v[142:143], v[146:147]
	v_pk_add_f32 v[22:23], v[22:23], v[24:25]
	v_pk_add_f32 v[140:141], v[140:141], v[142:143]
	v_pk_add_f32 v[138:139], v[138:139], v[22:23]
	v_add_u32_e32 v22, 0xffffe020, v2
	ds_read_b128 v[22:25], v22
	s_waitcnt lgkmcnt(0)
	v_pk_mul_f32 v[142:143], v[108:109], v[22:23] op_sel:[0,1]
	v_pk_mul_f32 v[144:145], v[106:107], v[22:23] op_sel:[0,1]
	v_pk_fma_f32 v[142:143], v[100:101], v[22:23], v[142:143] op_sel_hi:[1,0,1]
	v_pk_fma_f32 v[22:23], v[98:99], v[22:23], v[144:145] op_sel_hi:[1,0,1]
	v_mov_b32_e32 v144, v25
	v_pk_mul_f32 v[146:147], v[96:97], v[144:145] op_sel_hi:[1,0]
	v_pk_mul_f32 v[144:145], v[94:95], v[144:145] op_sel_hi:[1,0]
	v_pk_fma_f32 v[146:147], v[84:85], v[24:25], v[146:147] op_sel_hi:[1,0,1]
	v_pk_fma_f32 v[24:25], v[82:83], v[24:25], v[144:145] op_sel_hi:[1,0,1]
	v_pk_add_f32 v[142:143], v[142:143], v[146:147]
	v_pk_add_f32 v[22:23], v[22:23], v[24:25]
	v_pk_add_f32 v[140:141], v[140:141], v[142:143]
	v_pk_add_f32 v[138:139], v[138:139], v[22:23]
	v_add_u32_e32 v22, 0xffffe030, v2
	ds_read_b128 v[22:25], v22
	s_waitcnt lgkmcnt(0)
	v_pk_mul_f32 v[142:143], v[88:89], v[22:23] op_sel:[0,1]
	v_pk_mul_f32 v[144:145], v[86:87], v[22:23] op_sel:[0,1]
	v_pk_fma_f32 v[142:143], v[80:81], v[22:23], v[142:143] op_sel_hi:[1,0,1]
	v_pk_fma_f32 v[22:23], v[78:79], v[22:23], v[144:145] op_sel_hi:[1,0,1]
	v_mov_b32_e32 v144, v25
	v_pk_mul_f32 v[146:147], v[76:77], v[144:145] op_sel_hi:[1,0]
	v_pk_mul_f32 v[144:145], v[74:75], v[144:145] op_sel_hi:[1,0]
	v_pk_fma_f32 v[146:147], v[72:73], v[24:25], v[146:147] op_sel_hi:[1,0,1]
	v_pk_fma_f32 v[24:25], v[70:71], v[24:25], v[144:145] op_sel_hi:[1,0,1]
	v_pk_add_f32 v[142:143], v[142:143], v[146:147]
	v_pk_add_f32 v[22:23], v[22:23], v[24:25]
	v_pk_add_f32 v[24:25], v[140:141], v[142:143]
	v_pk_add_f32 v[22:23], v[138:139], v[22:23]
	v_add_u32_e32 v138, 0xfffff000, v2
	ds_read_b128 v[138:141], v138
	s_waitcnt lgkmcnt(0)
	v_pk_mul_f32 v[142:143], v[136:137], v[138:139] op_sel:[0,1]
	v_pk_mul_f32 v[144:145], v[134:135], v[138:139] op_sel:[0,1]
	v_pk_fma_f32 v[142:143], v[132:133], v[138:139], v[142:143] op_sel_hi:[1,0,1]
	v_pk_fma_f32 v[138:139], v[130:131], v[138:139], v[144:145] op_sel_hi:[1,0,1]
	v_mov_b32_e32 v144, v141
	v_pk_mul_f32 v[146:147], v[128:129], v[144:145] op_sel_hi:[1,0]
	v_pk_mul_f32 v[144:145], v[126:127], v[144:145] op_sel_hi:[1,0]
	v_pk_fma_f32 v[146:147], v[116:117], v[140:141], v[146:147] op_sel_hi:[1,0,1]
	v_pk_fma_f32 v[140:141], v[114:115], v[140:141], v[144:145] op_sel_hi:[1,0,1]
	v_pk_add_f32 v[142:143], v[142:143], v[146:147]
	v_pk_add_f32 v[138:139], v[138:139], v[140:141]
	v_pk_add_f32 v[140:141], v[8:9], v[142:143]
	v_pk_add_f32 v[138:139], v[6:7], v[138:139]
	v_add_u32_e32 v6, 0xfffff010, v2
	ds_read_b128 v[6:9], v6
	s_waitcnt lgkmcnt(0)
	v_pk_mul_f32 v[142:143], v[124:125], v[6:7] op_sel:[0,1]
	v_pk_mul_f32 v[144:145], v[122:123], v[6:7] op_sel:[0,1]
	v_pk_fma_f32 v[142:143], v[120:121], v[6:7], v[142:143] op_sel_hi:[1,0,1]
	v_pk_fma_f32 v[6:7], v[118:119], v[6:7], v[144:145] op_sel_hi:[1,0,1]
	v_mov_b32_e32 v144, v9
	v_pk_mul_f32 v[146:147], v[112:113], v[144:145] op_sel_hi:[1,0]
	v_pk_mul_f32 v[144:145], v[110:111], v[144:145] op_sel_hi:[1,0]
	v_pk_fma_f32 v[146:147], v[104:105], v[8:9], v[146:147] op_sel_hi:[1,0,1]
	v_pk_fma_f32 v[8:9], v[102:103], v[8:9], v[144:145] op_sel_hi:[1,0,1]
	v_pk_add_f32 v[142:143], v[142:143], v[146:147]
	v_pk_add_f32 v[6:7], v[6:7], v[8:9]
	v_pk_add_f32 v[140:141], v[140:141], v[142:143]
	v_pk_add_f32 v[138:139], v[138:139], v[6:7]
	v_add_u32_e32 v6, 0xfffff020, v2
	ds_read_b128 v[6:9], v6
	s_waitcnt lgkmcnt(0)
	v_pk_mul_f32 v[142:143], v[108:109], v[6:7] op_sel:[0,1]
	v_pk_mul_f32 v[144:145], v[106:107], v[6:7] op_sel:[0,1]
	v_pk_fma_f32 v[142:143], v[100:101], v[6:7], v[142:143] op_sel_hi:[1,0,1]
	v_pk_fma_f32 v[6:7], v[98:99], v[6:7], v[144:145] op_sel_hi:[1,0,1]
	v_mov_b32_e32 v144, v9
	v_pk_mul_f32 v[146:147], v[96:97], v[144:145] op_sel_hi:[1,0]
	v_pk_mul_f32 v[144:145], v[94:95], v[144:145] op_sel_hi:[1,0]
	v_pk_fma_f32 v[146:147], v[84:85], v[8:9], v[146:147] op_sel_hi:[1,0,1]
	v_pk_fma_f32 v[8:9], v[82:83], v[8:9], v[144:145] op_sel_hi:[1,0,1]
	v_pk_add_f32 v[142:143], v[142:143], v[146:147]
	v_pk_add_f32 v[6:7], v[6:7], v[8:9]
	v_pk_add_f32 v[140:141], v[140:141], v[142:143]
	v_pk_add_f32 v[138:139], v[138:139], v[6:7]
	v_add_u32_e32 v6, 0xfffff030, v2
	ds_read_b128 v[6:9], v6
	s_waitcnt lgkmcnt(0)
	v_pk_mul_f32 v[142:143], v[88:89], v[6:7] op_sel:[0,1]
	v_pk_mul_f32 v[144:145], v[86:87], v[6:7] op_sel:[0,1]
	v_pk_fma_f32 v[142:143], v[80:81], v[6:7], v[142:143] op_sel_hi:[1,0,1]
	v_pk_fma_f32 v[6:7], v[78:79], v[6:7], v[144:145] op_sel_hi:[1,0,1]
	v_mov_b32_e32 v144, v9
	v_pk_mul_f32 v[146:147], v[76:77], v[144:145] op_sel_hi:[1,0]
	v_pk_mul_f32 v[144:145], v[74:75], v[144:145] op_sel_hi:[1,0]
	v_pk_fma_f32 v[146:147], v[72:73], v[8:9], v[146:147] op_sel_hi:[1,0,1]
	v_pk_fma_f32 v[8:9], v[70:71], v[8:9], v[144:145] op_sel_hi:[1,0,1]
	v_pk_add_f32 v[142:143], v[142:143], v[146:147]
	v_pk_add_f32 v[6:7], v[6:7], v[8:9]
	v_pk_add_f32 v[8:9], v[140:141], v[142:143]
	v_pk_add_f32 v[6:7], v[138:139], v[6:7]
	ds_read_b128 v[150:153], v2
	ds_read_b128 v[146:149], v2 offset:16
	ds_read_b128 v[142:145], v2 offset:32
	ds_read_b128 v[138:141], v2 offset:48
	v_add_u32_e32 v2, 64, v2
	s_waitcnt lgkmcnt(3)
	v_pk_mul_f32 v[134:135], v[134:135], v[150:151] op_sel:[0,1]
	v_pk_mul_f32 v[136:137], v[136:137], v[150:151] op_sel:[0,1]
	v_pk_fma_f32 v[130:131], v[130:131], v[150:151], v[134:135] op_sel_hi:[1,0,1]
	v_mov_b32_e32 v134, v153
	v_pk_mul_f32 v[128:129], v[128:129], v[134:135] op_sel_hi:[1,0]
	v_pk_fma_f32 v[132:133], v[132:133], v[150:151], v[136:137] op_sel_hi:[1,0,1]
	v_pk_fma_f32 v[116:117], v[116:117], v[152:153], v[128:129] op_sel_hi:[1,0,1]
	v_pk_mul_f32 v[126:127], v[126:127], v[134:135] op_sel_hi:[1,0]
	v_pk_add_f32 v[116:117], v[132:133], v[116:117]
	v_pk_fma_f32 v[114:115], v[114:115], v[152:153], v[126:127] op_sel_hi:[1,0,1]
	v_pk_add_f32 v[92:93], v[92:93], v[116:117]
	s_waitcnt lgkmcnt(2)
	v_pk_mul_f32 v[116:117], v[122:123], v[146:147] op_sel:[0,1]
	v_pk_add_f32 v[114:115], v[130:131], v[114:115]
	v_pk_fma_f32 v[116:117], v[118:119], v[146:147], v[116:117] op_sel_hi:[1,0,1]
	v_mov_b32_e32 v118, v149
	v_pk_add_f32 v[114:115], v[90:91], v[114:115]
	v_pk_mul_f32 v[90:91], v[124:125], v[146:147] op_sel:[0,1]
	v_pk_mul_f32 v[112:113], v[112:113], v[118:119] op_sel_hi:[1,0]
	v_pk_mul_f32 v[110:111], v[110:111], v[118:119] op_sel_hi:[1,0]
	v_pk_fma_f32 v[90:91], v[120:121], v[146:147], v[90:91] op_sel_hi:[1,0,1]
	v_pk_fma_f32 v[104:105], v[104:105], v[148:149], v[112:113] op_sel_hi:[1,0,1]
	v_pk_fma_f32 v[102:103], v[102:103], v[148:149], v[110:111] op_sel_hi:[1,0,1]
	v_pk_add_f32 v[90:91], v[90:91], v[104:105]
	v_pk_add_f32 v[102:103], v[116:117], v[102:103]
	v_pk_add_f32 v[90:91], v[92:93], v[90:91]
	v_pk_add_f32 v[92:93], v[114:115], v[102:103]
	s_waitcnt lgkmcnt(1)
	v_pk_mul_f32 v[102:103], v[108:109], v[142:143] op_sel:[0,1]
	s_waitcnt lgkmcnt(0)
	v_pk_mul_f32 v[86:87], v[86:87], v[138:139] op_sel:[0,1]
	v_pk_fma_f32 v[100:101], v[100:101], v[142:143], v[102:103] op_sel_hi:[1,0,1]
	v_mov_b32_e32 v102, v145
	v_pk_mul_f32 v[104:105], v[106:107], v[142:143] op_sel:[0,1]
	v_pk_mul_f32 v[96:97], v[96:97], v[102:103] op_sel_hi:[1,0]
	v_pk_mul_f32 v[94:95], v[94:95], v[102:103] op_sel_hi:[1,0]
	v_pk_fma_f32 v[78:79], v[78:79], v[138:139], v[86:87] op_sel_hi:[1,0,1]
	v_mov_b32_e32 v86, v141
	v_pk_fma_f32 v[98:99], v[98:99], v[142:143], v[104:105] op_sel_hi:[1,0,1]
	v_pk_fma_f32 v[84:85], v[84:85], v[144:145], v[96:97] op_sel_hi:[1,0,1]
	v_pk_fma_f32 v[82:83], v[82:83], v[144:145], v[94:95] op_sel_hi:[1,0,1]
	v_pk_mul_f32 v[88:89], v[88:89], v[138:139] op_sel:[0,1]
	v_pk_mul_f32 v[76:77], v[76:77], v[86:87] op_sel_hi:[1,0]
	v_pk_mul_f32 v[74:75], v[74:75], v[86:87] op_sel_hi:[1,0]
	v_pk_add_f32 v[84:85], v[100:101], v[84:85]
	v_pk_add_f32 v[94:95], v[98:99], v[82:83]
	v_pk_fma_f32 v[80:81], v[80:81], v[138:139], v[88:89] op_sel_hi:[1,0,1]
	v_pk_fma_f32 v[72:73], v[72:73], v[140:141], v[76:77] op_sel_hi:[1,0,1]
	v_pk_fma_f32 v[70:71], v[70:71], v[140:141], v[74:75] op_sel_hi:[1,0,1]
	v_pk_add_f32 v[82:83], v[90:91], v[84:85]
	v_pk_add_f32 v[84:85], v[92:93], v[94:95]
	v_pk_add_f32 v[72:73], v[80:81], v[72:73]
	v_pk_add_f32 v[70:71], v[78:79], v[70:71]
	v_pk_add_f32 v[92:93], v[82:83], v[72:73]
	v_pk_add_f32 v[90:91], v[84:85], v[70:71]
	s_cbranch_scc0 .LBB0_15
	s_movk_i32 s31, 0x400
	s_mov_b64 s[36:37], 0
	s_and_b64 vcc, exec, s[34:35]
	s_cbranch_vccz .LBB0_12
	ds_bpermute_b32 v4, v166, v66
	ds_bpermute_b32 v5, v166, v67
	ds_bpermute_b32 v70, v166, v68
	ds_bpermute_b32 v71, v166, v69
	s_waitcnt lgkmcnt(0)
	s_barrier
	s_and_saveexec_b64 s[34:35], s[8:9]
	v_pk_add_f32 v[68:69], v[68:69], v[70:71]
	v_pk_add_f32 v[66:67], v[66:67], v[4:5]
	ds_write_b128 v170, v[66:69]
	s_or_b64 exec, exec, s[34:35]
	ds_bpermute_b32 v4, v166, v62
	ds_bpermute_b32 v5, v166, v63
	ds_bpermute_b32 v66, v166, v64
	ds_bpermute_b32 v67, v166, v65
	s_and_saveexec_b64 s[34:35], s[8:9]
	s_cbranch_execz .LBB0_21
	s_waitcnt lgkmcnt(0)
	v_pk_add_f32 v[64:65], v[64:65], v[66:67]
	v_pk_add_f32 v[62:63], v[62:63], v[4:5]
	ds_write_b128 v170, v[62:65] offset:512

.LBB0_171:
	s_andn2_b64 vcc, exec, s[8:9]
	s_cbranch_vccnz .LBB0_60
	s_mov_b64 s[8:9], -1
	s_cmp_gt_i32 s33, -1
	v_add_u32_e32 v127, 0x2100, v83
	v_add_u32_e32 v126, 0x2108, v83
	v_add_u32_e32 v125, 0x2520, v83
	v_add_u32_e32 v124, 0x2528, v83
	v_add_u32_e32 v123, 0x2940, v83
	v_add_u32_e32 v122, 0x2948, v83
	v_add_u32_e32 v121, 0x2d60, v83
	v_add_u32_e32 v120, 0x2d68, v83
	v_add_u32_e32 v119, 0x3180, v83
	v_add_u32_e32 v118, 0x3188, v83
	v_add_u32_e32 v117, 0x35a0, v83
	v_add_u32_e32 v116, 0x35a8, v83
	v_add_u32_e32 v115, 0x39c0, v83
	v_add_u32_e32 v114, 0x39c8, v83
	v_add_u32_e32 v113, 0x3de0, v83
	v_add_u32_e32 v112, 0x3de8, v83
	v_add_u32_e32 v111, 0x400, v88
	s_cbranch_scc0 .LBB0_174
	v_readlane_b32 s36, v254, 10
	v_readlane_b32 s37, v254, 11
	s_load_dwordx2 s[36:37], s[36:37], 0xd0
	s_and_b32 s8, s50, 0x7e0
	s_and_b32 s30, s48, 0x1ff80
	v_or_b32_e32 v2, s8, v82
	v_or_b32_e32 v4, s30, v81
	v_lshlrev_b32_e32 v2, 2, v2
	v_mov_b32_e32 v3, v69
	s_waitcnt lgkmcnt(0)
	v_lshl_add_u64 v[2:3], s[36:37], 0, v[2:3]
	v_lshlrev_b32_e32 v4, 13, v4
	v_mov_b32_e32 v5, v69
	v_lshl_add_u64 v[62:63], v[2:3], 0, v[4:5]
	v_add_co_u32_e32 v6, vcc, 0x10000, v62
	s_nop 1
	v_addc_co_u32_e32 v7, vcc, 0, v63, vcc
	global_load_dwordx4 v[2:5], v[62:63], off
	s_nop 0
	global_load_dwordx4 v[6:9], v[6:7], off
	v_add_co_u32_e32 v10, vcc, 0x20000, v62
	s_nop 0
	s_nop 0
	v_addc_co_u32_e32 v11, vcc, 0, v63, vcc
	v_add_co_u32_e32 v14, vcc, 0x30000, v62
	s_nop 1
	v_addc_co_u32_e32 v15, vcc, 0, v63, vcc
	global_load_dwordx4 v[10:13], v[10:11], off
	s_nop 0
	global_load_dwordx4 v[14:17], v[14:15], off
	v_add_co_u32_e32 v18, vcc, 0x40000, v62
	s_nop 1
	v_addc_co_u32_e32 v19, vcc, 0, v63, vcc
	v_add_co_u32_e32 v22, vcc, 0x50000, v62
	s_nop 1
	v_addc_co_u32_e32 v23, vcc, 0, v63, vcc
	global_load_dwordx4 v[18:21], v[18:19], off
	s_nop 0
	global_load_dwordx4 v[22:25], v[22:23], off
	v_add_co_u32_e32 v26, vcc, 0x60000, v62
	s_nop 1
	v_addc_co_u32_e32 v27, vcc, 0, v63, vcc
	v_add_co_u32_e32 v30, vcc, 0x70000, v62
	s_nop 1
	v_addc_co_u32_e32 v31, vcc, 0, v63, vcc
	global_load_dwordx4 v[26:29], v[26:27], off
	s_nop 0
	global_load_dwordx4 v[30:33], v[30:31], off
	v_add_co_u32_e32 v34, vcc, 0x80000, v62
	s_nop 1
	v_addc_co_u32_e32 v35, vcc, 0, v63, vcc
	v_add_co_u32_e32 v38, vcc, 0x90000, v62
	s_nop 1
	v_addc_co_u32_e32 v39, vcc, 0, v63, vcc
	global_load_dwordx4 v[34:37], v[34:35], off
	s_nop 0
	global_load_dwordx4 v[38:41], v[38:39], off
	v_add_co_u32_e32 v42, vcc, 0xa0000, v62
	s_nop 1
	v_addc_co_u32_e32 v43, vcc, 0, v63, vcc
	v_add_co_u32_e32 v46, vcc, 0xb0000, v62
	s_nop 1
	v_addc_co_u32_e32 v47, vcc, 0, v63, vcc
	global_load_dwordx4 v[42:45], v[42:43], off
	s_nop 0
	global_load_dwordx4 v[46:49], v[46:47], off
	v_add_co_u32_e32 v50, vcc, 0xc0000, v62
	s_nop 1
	v_addc_co_u32_e32 v51, vcc, 0, v63, vcc
	v_add_co_u32_e32 v54, vcc, 0xd0000, v62
	s_nop 1
	v_addc_co_u32_e32 v55, vcc, 0, v63, vcc
	global_load_dwordx4 v[50:53], v[50:51], off
	s_nop 0
	global_load_dwordx4 v[54:57], v[54:55], off
	v_add_co_u32_e32 v58, vcc, 0xe0000, v62
	s_nop 0
	s_nop 0
	v_addc_co_u32_e32 v59, vcc, 0, v63, vcc
	global_load_dwordx4 v[58:61], v[58:59], off
	v_add_co_u32_e32 v62, vcc, 0xf0000, v62
	s_nop 0
	s_nop 0
	v_addc_co_u32_e32 v63, vcc, 0, v63, vcc
	global_load_dwordx4 v[62:65], v[62:63], off
	s_waitcnt vmcnt(15)
	v_pk_mul_f32 v[2:3], v[2:3], s[34:35] op_sel_hi:[1,0]
	ds_write2_b32 v83, v2, v3 offset1:1
	v_pk_mul_f32 v[2:3], v[4:5], s[34:35] op_sel_hi:[1,0]
	ds_write2_b32 v83, v2, v3 offset0:2 offset1:3
	s_waitcnt vmcnt(14)
	v_pk_mul_f32 v[2:3], v[6:7], s[34:35] op_sel_hi:[1,0]
	ds_write2_b32 v89, v2, v3 offset1:1
	v_pk_mul_f32 v[2:3], v[8:9], s[34:35] op_sel_hi:[1,0]
	ds_write2_b32 v90, v2, v3 offset1:1
	v_mov_b32_e32 v5, v69
	v_lshl_add_u64 v[6:7], v[74:75], 0, s[30:31]
	s_waitcnt vmcnt(13)
	v_pk_mul_f32 v[2:3], v[10:11], s[34:35] op_sel_hi:[1,0]
	ds_write2_b32 v91, v2, v3 offset1:1
	v_pk_mul_f32 v[2:3], v[12:13], s[34:35] op_sel_hi:[1,0]
	ds_write2_b32 v92, v2, v3 offset1:1
	s_waitcnt vmcnt(12)
	v_pk_mul_f32 v[2:3], v[14:15], s[34:35] op_sel_hi:[1,0]
	ds_write2_b32 v93, v2, v3 offset1:1
	v_pk_mul_f32 v[2:3], v[16:17], s[34:35] op_sel_hi:[1,0]
	ds_write2_b32 v94, v2, v3 offset1:1
	s_waitcnt vmcnt(11)
	v_pk_mul_f32 v[2:3], v[18:19], s[34:35] op_sel_hi:[1,0]
	ds_write2_b32 v95, v2, v3 offset1:1
	v_pk_mul_f32 v[2:3], v[20:21], s[34:35] op_sel_hi:[1,0]
	ds_write2_b32 v96, v2, v3 offset1:1
	s_waitcnt vmcnt(10)
	v_pk_mul_f32 v[2:3], v[22:23], s[34:35] op_sel_hi:[1,0]
	ds_write2_b32 v97, v2, v3 offset1:1
	v_pk_mul_f32 v[2:3], v[24:25], s[34:35] op_sel_hi:[1,0]
	ds_write2_b32 v98, v2, v3 offset1:1
	s_waitcnt vmcnt(9)
	v_pk_mul_f32 v[2:3], v[26:27], s[34:35] op_sel_hi:[1,0]
	ds_write2_b32 v99, v2, v3 offset1:1
	v_pk_mul_f32 v[2:3], v[28:29], s[34:35] op_sel_hi:[1,0]
	ds_write2_b32 v100, v2, v3 offset1:1
	s_waitcnt vmcnt(8)
	v_pk_mul_f32 v[2:3], v[30:31], s[34:35] op_sel_hi:[1,0]
	ds_write2_b32 v101, v2, v3 offset1:1
	v_pk_mul_f32 v[2:3], v[32:33], s[34:35] op_sel_hi:[1,0]
	ds_write2_b32 v102, v2, v3 offset1:1
	s_waitcnt vmcnt(7)
	v_pk_mul_f32 v[2:3], v[34:35], s[34:35] op_sel_hi:[1,0]
	ds_write2_b32 v127, v2, v3 offset1:1
	v_pk_mul_f32 v[2:3], v[36:37], s[34:35] op_sel_hi:[1,0]
	ds_write2_b32 v126, v2, v3 offset1:1
	s_waitcnt vmcnt(6)
	v_pk_mul_f32 v[2:3], v[38:39], s[34:35] op_sel_hi:[1,0]
	ds_write2_b32 v125, v2, v3 offset1:1
	v_pk_mul_f32 v[2:3], v[40:41], s[34:35] op_sel_hi:[1,0]
	ds_write2_b32 v124, v2, v3 offset1:1
	v_or_b32_e32 v40, s8, v81
	v_mul_u32_u24_e32 v40, 0x1600, v40
	v_mov_b32_e32 v41, v69
	s_waitcnt vmcnt(5)
	v_pk_mul_f32 v[2:3], v[42:43], s[34:35] op_sel_hi:[1,0]
	ds_write2_b32 v123, v2, v3 offset1:1
	v_pk_mul_f32 v[2:3], v[44:45], s[34:35] op_sel_hi:[1,0]
	ds_write2_b32 v122, v2, v3 offset1:1
	s_waitcnt vmcnt(4)
	v_pk_mul_f32 v[2:3], v[46:47], s[34:35] op_sel_hi:[1,0]
	ds_write2_b32 v121, v2, v3 offset1:1
	v_pk_mul_f32 v[2:3], v[48:49], s[34:35] op_sel_hi:[1,0]
	ds_write2_b32 v120, v2, v3 offset1:1
	v_lshl_add_u64 v[40:41], v[6:7], 0, v[40:41]
	s_waitcnt vmcnt(3)
	v_pk_mul_f32 v[2:3], v[50:51], s[34:35] op_sel_hi:[1,0]
	ds_write2_b32 v119, v2, v3 offset1:1
	v_pk_mul_f32 v[2:3], v[52:53], s[34:35] op_sel_hi:[1,0]
	ds_write2_b32 v118, v2, v3 offset1:1
	s_waitcnt vmcnt(2)
	v_pk_mul_f32 v[2:3], v[54:55], s[34:35] op_sel_hi:[1,0]
	ds_write2_b32 v117, v2, v3 offset1:1
	v_pk_mul_f32 v[2:3], v[56:57], s[34:35] op_sel_hi:[1,0]
	ds_write2_b32 v116, v2, v3 offset1:1
	s_waitcnt vmcnt(1)
	v_pk_mul_f32 v[2:3], v[58:59], s[34:35] op_sel_hi:[1,0]
	ds_write2_b32 v115, v2, v3 offset1:1
	v_pk_mul_f32 v[2:3], v[60:61], s[34:35] op_sel_hi:[1,0]
	ds_write2_b32 v114, v2, v3 offset1:1
	s_waitcnt vmcnt(0)
	v_pk_mul_f32 v[2:3], v[62:63], s[34:35] op_sel_hi:[1,0]
	ds_write2_b32 v113, v2, v3 offset1:1
	v_pk_mul_f32 v[2:3], v[64:65], s[34:35] op_sel_hi:[1,0]
	ds_write2_b32 v112, v2, v3 offset1:1
	s_waitcnt lgkmcnt(0)
	ds_read2_b32 v[8:9], v111 offset0:206 offset1:214
	ds_read2_b32 v[10:11], v111 offset0:239 offset1:247
	ds_read2_b32 v[12:13], v111 offset0:140 offset1:148
	ds_read2_b32 v[14:15], v111 offset0:173 offset1:181
	ds_read2_b32 v[16:17], v111 offset0:74 offset1:82
	ds_read2_b32 v[18:19], v111 offset0:107 offset1:115
	ds_read2_b32 v[20:21], v111 offset0:8 offset1:16
	ds_read2_b32 v[22:23], v111 offset0:41 offset1:49
	s_waitcnt lgkmcnt(7)
	v_med3_f32 v2, v8, s53, v103
	s_waitcnt lgkmcnt(6)
	v_med3_f32 v3, v10, s53, v103
	s_waitcnt lgkmcnt(5)
	v_med3_f32 v4, v12, s53, v103
	s_waitcnt lgkmcnt(4)
	v_med3_f32 v8, v14, s53, v103
	v_cvt_pk_fp8_f32 v5, v4, v8
	s_waitcnt lgkmcnt(1)
	v_med3_f32 v8, v20, s53, v103
	s_waitcnt lgkmcnt(0)
	v_med3_f32 v10, v22, s53, v103
	v_mov_b32_e32 v4, v69
	ds_read2_b32 v[24:25], v88 offset0:198 offset1:206
	ds_read2_b32 v[26:27], v88 offset0:231 offset1:239
	ds_read2_b32 v[28:29], v88 offset0:132 offset1:140
	ds_read2_b32 v[30:31], v88 offset0:165 offset1:173
	v_cvt_pk_fp8_f32 v4, v8, v10
	ds_read2_b32 v[32:33], v88 offset1:8
	ds_read2_b32 v[34:35], v88 offset0:33 offset1:41
	v_cvt_pk_fp8_f32 v5, v2, v3 op_sel:[0,0,1]
	v_med3_f32 v2, v16, s53, v103
	v_med3_f32 v3, v18, s53, v103
	v_cvt_pk_fp8_f32 v4, v2, v3 op_sel:[0,0,1]
	s_waitcnt lgkmcnt(3)
	v_med3_f32 v2, v28, s53, v103
	s_waitcnt lgkmcnt(2)
	v_med3_f32 v12, v30, s53, v103
	v_mov_b32_e32 v3, v69
	ds_read2_b32 v[36:37], v88 offset0:66 offset1:74
	ds_read2_b32 v[38:39], v88 offset0:99 offset1:107
	v_cvt_pk_fp8_f32 v3, v2, v12
	s_waitcnt lgkmcnt(3)
	v_med3_f32 v12, v32, s53, v103
	s_waitcnt lgkmcnt(2)
	v_med3_f32 v14, v34, s53, v103
	v_mov_b32_e32 v2, v69
	v_cvt_pk_fp8_f32 v2, v12, v14
	v_med3_f32 v8, v24, s53, v103
	v_med3_f32 v10, v26, s53, v103
	v_cvt_pk_fp8_f32 v3, v8, v10 op_sel:[0,0,1]
	s_waitcnt lgkmcnt(1)
	v_med3_f32 v8, v36, s53, v103
	s_waitcnt lgkmcnt(0)
	v_med3_f32 v10, v38, s53, v103
	v_cvt_pk_fp8_f32 v2, v8, v10 op_sel:[0,0,1]
	v_med3_f32 v10, v23, s53, v103
	v_med3_f32 v12, v35, s53, v103
	v_or_b32_e32 v8, s8, v84
	global_store_dwordx4 v[40:41], v[2:5], off
	v_mul_u32_u24_e32 v8, 0x1600, v8
	v_or_b32_e32 v40, s8, v85
	v_med3_f32 v2, v9, s53, v103
	v_med3_f32 v4, v13, s53, v103
	v_med3_f32 v9, v15, s53, v103
	v_mov_b32_e32 v5, v69
	v_cvt_pk_fp8_f32 v5, v4, v9
	v_med3_f32 v9, v21, s53, v103
	v_mov_b32_e32 v4, v69
	v_cvt_pk_fp8_f32 v4, v9, v10
	v_med3_f32 v3, v11, s53, v103
	v_cvt_pk_fp8_f32 v5, v2, v3 op_sel:[0,0,1]
	v_med3_f32 v2, v17, s53, v103
	v_med3_f32 v3, v19, s53, v103
	v_cvt_pk_fp8_f32 v4, v2, v3 op_sel:[0,0,1]
	v_med3_f32 v2, v29, s53, v103
	v_med3_f32 v11, v31, s53, v103
	v_mov_b32_e32 v3, v69
	v_cvt_pk_fp8_f32 v3, v2, v11
	v_med3_f32 v11, v33, s53, v103
	v_mov_b32_e32 v2, v69
	v_cvt_pk_fp8_f32 v2, v11, v12
	v_med3_f32 v9, v25, s53, v103
	v_med3_f32 v10, v27, s53, v103
	v_cvt_pk_fp8_f32 v3, v9, v10 op_sel:[0,0,1]
	v_med3_f32 v9, v37, s53, v103
	v_med3_f32 v10, v39, s53, v103
	v_cvt_pk_fp8_f32 v2, v9, v10 op_sel:[0,0,1]
	v_mov_b32_e32 v9, v69
	v_lshl_add_u64 v[8:9], v[6:7], 0, v[8:9]
	v_mul_u32_u24_e32 v40, 0x1600, v40
	global_store_dwordx4 v[8:9], v[2:5], off
	ds_read2_b32 v[8:9], v111 offset0:222 offset1:230
	v_mov_b32_e32 v41, v69
	v_add_u32_e32 v2, 0x600, v88
	ds_read2_b32 v[10:11], v2 offset0:127 offset1:135
	ds_read2_b32 v[12:13], v111 offset0:156 offset1:164
	ds_read2_b32 v[14:15], v111 offset0:189 offset1:197
	ds_read2_b32 v[16:17], v111 offset0:90 offset1:98
	ds_read2_b32 v[18:19], v111 offset0:123 offset1:131
	ds_read2_b32 v[20:21], v111 offset0:24 offset1:32
	ds_read2_b32 v[22:23], v111 offset0:57 offset1:65
	s_waitcnt lgkmcnt(7)
	v_med3_f32 v2, v8, s53, v103
	v_mov_b32_e32 v5, v69
	s_waitcnt lgkmcnt(5)
	v_med3_f32 v4, v12, s53, v103
	s_waitcnt lgkmcnt(4)
	v_med3_f32 v8, v14, s53, v103
	v_med3_f32 v3, v10, s53, v103
	v_cvt_pk_fp8_f32 v5, v4, v8
	s_waitcnt lgkmcnt(1)
	v_med3_f32 v8, v20, s53, v103
	s_waitcnt lgkmcnt(0)
	v_med3_f32 v10, v22, s53, v103
	v_mov_b32_e32 v4, v69
	ds_read2_b32 v[24:25], v88 offset0:214 offset1:222
	ds_read2_b32 v[26:27], v88 offset0:247 offset1:255
	ds_read2_b32 v[28:29], v88 offset0:148 offset1:156
	ds_read2_b32 v[30:31], v88 offset0:181 offset1:189
	v_cvt_pk_fp8_f32 v4, v8, v10
	ds_read2_b32 v[32:33], v88 offset0:16 offset1:24
	ds_read2_b32 v[34:35], v88 offset0:49 offset1:57
	v_cvt_pk_fp8_f32 v5, v2, v3 op_sel:[0,0,1]
	v_med3_f32 v2, v16, s53, v103
	v_med3_f32 v3, v18, s53, v103
	v_cvt_pk_fp8_f32 v4, v2, v3 op_sel:[0,0,1]
	s_waitcnt lgkmcnt(3)
	v_med3_f32 v2, v28, s53, v103
	s_waitcnt lgkmcnt(2)
	v_med3_f32 v12, v30, s53, v103
	v_mov_b32_e32 v3, v69
	ds_read2_b32 v[36:37], v88 offset0:82 offset1:90
	ds_read2_b32 v[38:39], v88 offset0:115 offset1:123
	v_cvt_pk_fp8_f32 v3, v2, v12
	s_waitcnt lgkmcnt(3)
	v_med3_f32 v12, v32, s53, v103
	s_waitcnt lgkmcnt(2)
	v_med3_f32 v14, v34, s53, v103
	v_mov_b32_e32 v2, v69
	v_cvt_pk_fp8_f32 v2, v12, v14
	v_med3_f32 v8, v24, s53, v103
	v_med3_f32 v10, v26, s53, v103
	v_cvt_pk_fp8_f32 v3, v8, v10 op_sel:[0,0,1]
	s_waitcnt lgkmcnt(1)
	v_med3_f32 v8, v36, s53, v103
	s_waitcnt lgkmcnt(0)
	v_med3_f32 v10, v38, s53, v103
	v_cvt_pk_fp8_f32 v2, v8, v10 op_sel:[0,0,1]
	v_lshl_add_u64 v[40:41], v[6:7], 0, v[40:41]
	v_med3_f32 v10, v23, s53, v103
	v_med3_f32 v12, v35, s53, v103
	global_store_dwordx4 v[40:41], v[2:5], off
	v_or_b32_e32 v8, s8, v86
	v_mul_u32_u24_e32 v8, 0x1600, v8
	v_med3_f32 v2, v9, s53, v103
	v_med3_f32 v4, v13, s53, v103
	v_med3_f32 v9, v15, s53, v103
	v_mov_b32_e32 v5, v69
	v_cvt_pk_fp8_f32 v5, v4, v9
	v_med3_f32 v9, v21, s53, v103
	v_mov_b32_e32 v4, v69
	v_cvt_pk_fp8_f32 v4, v9, v10
	v_med3_f32 v3, v11, s53, v103
	v_cvt_pk_fp8_f32 v5, v2, v3 op_sel:[0,0,1]
	v_med3_f32 v2, v17, s53, v103
	v_med3_f32 v3, v19, s53, v103
	v_cvt_pk_fp8_f32 v4, v2, v3 op_sel:[0,0,1]
	v_med3_f32 v2, v29, s53, v103
	v_med3_f32 v11, v31, s53, v103
	v_mov_b32_e32 v3, v69
	v_cvt_pk_fp8_f32 v3, v2, v11
	v_med3_f32 v11, v33, s53, v103
	v_mov_b32_e32 v2, v69
	v_cvt_pk_fp8_f32 v2, v11, v12
	v_med3_f32 v9, v25, s53, v103
	v_med3_f32 v10, v27, s53, v103
	v_cvt_pk_fp8_f32 v3, v9, v10 op_sel:[0,0,1]
	v_med3_f32 v9, v37, s53, v103
	v_med3_f32 v10, v39, s53, v103
	v_cvt_pk_fp8_f32 v2, v9, v10 op_sel:[0,0,1]
	v_mov_b32_e32 v9, v69
	v_lshl_add_u64 v[6:7], v[6:7], 0, v[8:9]
	s_mov_b64 s[8:9], 0
	global_store_dwordx4 v[6:7], v[2:5], off
	s_waitcnt lgkmcnt(0)
